# baseline (speedup 1.0000x reference)
_Z12k1_colsum_q8PKfPjPfS2_:
	s_load_dwordx8 s[4:11], s[0:1], 0x0
	v_and_b32_e32 v1, 63, v0
	v_lshrrev_b32_e32 v41, 6, v0
	s_mul_i32 s12, s2, 0xc35
	s_lshr_b32 s12, s12, 4
	v_readfirstlane_b32 s14, v41
	s_add_i32 s13, s2, 1
	s_mul_i32 s13, s13, 0xc35
	s_lshr_b32 s13, s13, 4
	s_sub_u32 s13, s13, s12
	s_sub_u32 s15, s13, 0xc0
	s_cmp_lt_u32 s14, s15
	s_cselect_b32 s29, 1, 0
	v_lshlrev_b32_e32 v34, 4, v1
	v_min_u32_e32 v35, 57, v1
	v_lshlrev_b32_e32 v35, 4, v35
	v_cmp_gt_u32_e64 s[18:19], 58, v1
	s_lshl_b32 s35, s14, 13
	s_add_u32 s36, s35, 0x1000
	v_add_u32_e32 v38, s35, v34
	v_lshrrev_b32_e32 v41, 5, v1
	v_mov_b32_e32 v42, 0xc35000
	v_mul_lo_u32 v39, v41, v42
	v_and_b32_e32 v42, 31, v1
	v_lshl_add_u32 v39, v42, 2, v39
	v_mov_b32_e32 v2, 0
	v_mov_b32_e32 v3, 0
	v_mov_b32_e32 v4, 0
	v_mov_b32_e32 v5, 0
	v_mov_b32_e32 v6, 0
	v_mov_b32_e32 v7, 0
	v_mov_b32_e32 v8, 0
	v_mov_b32_e32 v9, 0
	v_mov_b32_e32 v10, 0
	v_mov_b32_e32 v11, 0
	v_mov_b32_e32 v12, 0
	v_mov_b32_e32 v13, 0
	v_mov_b32_e32 v14, 0
	v_mov_b32_e32 v15, 0
	v_mov_b32_e32 v16, 0
	v_mov_b32_e32 v17, 0
	v_mov_b32_e32 v40, 0
	v_mov_b32_e32 v47, 0x42fe0000
	s_mov_b32 s32, 0x42fe0000
	s_mov_b32 s33, 0xc0c0400
	s_mov_b32 s34, 0x4000c0c
	s_add_u32 s15, s12, s14
	s_mul_i32 s37, s15, 0xfa0
	s_lshl_b32 s15, s15, 7
	s_waitcnt lgkmcnt(0)
	s_add_u32 s16, s4, s37
	s_addc_u32 s17, s5, 0
	s_add_u32 s40, s6, s15
	s_addc_u32 s41, s7, 0
	s_add_u32 s20, s40, 0
	s_addc_u32 s21, s41, 0
	s_add_u32 s22, s20, 0x186a000
	s_addc_u32 s23, s21, 0
	s_add_u32 s24, s22, 0x186a000
	s_addc_u32 s25, s23, 0
	s_add_u32 s26, s24, 0x186a000
	s_addc_u32 s27, s25, 0
	s_mov_b32 m0, s35
	s_nop 0
	global_load_lds_dwordx4 v34, s[16:17] nt
	global_load_lds_dwordx4 v34, s[16:17] offset:1024 nt
	global_load_lds_dwordx4 v34, s[16:17] offset:2048 nt
	global_load_lds_dwordx4 v35, s[16:17] offset:3072 nt
	s_add_u32 s16, s16, 0x7d00
	s_addc_u32 s17, s17, 0
	s_waitcnt vmcnt(0)
	ds_read_b128 v[18:21], v38 offset:0
	ds_read_b128 v[22:25], v38 offset:1024
	ds_read_b128 v[26:29], v38 offset:2048
	ds_read_b128 v[30:33], v38 offset:3072
	s_waitcnt lgkmcnt(0)
	s_mov_b32 m0, s36
	s_nop 0
	global_load_lds_dwordx4 v34, s[16:17] nt
	global_load_lds_dwordx4 v34, s[16:17] offset:1024 nt
	global_load_lds_dwordx4 v34, s[16:17] offset:2048 nt
	global_load_lds_dwordx4 v35, s[16:17] offset:3072 nt
	s_add_u32 s16, s16, 0x7d00
	s_addc_u32 s17, s17, 0
	v_cndmask_b32_e64 v30, 0, v30, s[18:19]
	v_cndmask_b32_e64 v31, 0, v31, s[18:19]
	v_cndmask_b32_e64 v32, 0, v32, s[18:19]
	v_cndmask_b32_e64 v33, 0, v33, s[18:19]
	v_max3_f32 v41, |v18|, |v19|, |v20|
	v_max3_f32 v42, |v21|, |v22|, |v23|
	v_max3_f32 v43, |v24|, |v25|, |v26|
	v_max3_f32 v44, |v27|, |v28|, |v29|
	v_max3_f32 v48, |v30|, |v31|, |v32|
	v_max3_f32 v41, v41, v42, |v33|
	v_max3_f32 v43, v43, v44, v48
	v_max_f32_e32 v41, v41, v43
	v_pk_add_f32 v[2:3], v[2:3], v[18:19]
	v_pk_add_f32 v[4:5], v[4:5], v[20:21]
	v_max_f32_dpp v41, v41, v41 quad_perm:[1,0,3,2] row_mask:0xf bank_mask:0xf
	v_pk_add_f32 v[6:7], v[6:7], v[22:23]
	v_pk_add_f32 v[8:9], v[8:9], v[24:25]
	v_max_f32_dpp v41, v41, v41 quad_perm:[2,3,0,1] row_mask:0xf bank_mask:0xf
	v_pk_add_f32 v[10:11], v[10:11], v[26:27]
	v_pk_add_f32 v[12:13], v[12:13], v[28:29]
	v_max_f32_dpp v41, v41, v41 row_half_mirror row_mask:0xf bank_mask:0xf
	v_pk_add_f32 v[14:15], v[14:15], v[30:31]
	v_pk_add_f32 v[16:17], v[16:17], v[32:33]
	v_max_f32_dpp v41, v41, v41 row_mirror row_mask:0xf bank_mask:0xf
	s_nop 1
	v_max_f32_dpp v41, v41, v41 row_bcast:15 row_mask:0xa bank_mask:0xf
	s_nop 1
	v_max_f32_dpp v41, v41, v41 row_bcast:31 row_mask:0xc bank_mask:0xf
	s_nop 1
	v_readlane_b32 s28, v41, 63
	s_nop 1
	v_div_scale_f32 v48, s[30:31], s28, s28, v47
	v_rcp_f32_e32 v49, v48
	s_nop 0
	v_fma_f32 v50, -v48, v49, 1.0
	v_fmac_f32_e32 v49, v50, v49
	v_mov_b32_e32 v50, s28
	v_div_scale_f32 v50, vcc, s32, v50, s32
	v_mul_f32_e32 v51, v50, v49
	v_fma_f32 v52, -v48, v51, v50
	v_fmac_f32_e32 v51, v52, v49
	v_fma_f32 v48, -v48, v51, v50
	v_div_fmas_f32 v48, v48, v49, v51
	v_div_fixup_f32 v48, v48, s28, v47
	v_cmp_gt_f32_e64 vcc, s28, 0
	v_writelane_b32 v40, s28, 0
	s_nop 0
	v_cndmask_b32_e32 v48, 0, v48, vcc
	v_fmaak_f32 v49, v18, v48, 0x4b400000
	v_fmaak_f32 v50, v19, v48, 0x4b400000
	v_fmaak_f32 v51, v20, v48, 0x4b400000
	v_fmaak_f32 v52, v21, v48, 0x4b400000
	v_perm_b32 v49, v50, v49, s33
	v_perm_b32 v51, v52, v51, s34
	v_or_b32_e32 v56, v49, v51
	v_fmaak_f32 v41, v22, v48, 0x4b400000
	v_fmaak_f32 v42, v23, v48, 0x4b400000
	v_fmaak_f32 v43, v24, v48, 0x4b400000
	v_fmaak_f32 v44, v25, v48, 0x4b400000
	v_perm_b32 v41, v42, v41, s33
	v_perm_b32 v43, v44, v43, s34
	v_or_b32_e32 v57, v41, v43
	v_fmaak_f32 v49, v26, v48, 0x4b400000
	v_fmaak_f32 v50, v27, v48, 0x4b400000
	v_fmaak_f32 v51, v28, v48, 0x4b400000
	v_fmaak_f32 v52, v29, v48, 0x4b400000
	v_perm_b32 v49, v50, v49, s33
	v_perm_b32 v51, v52, v51, s34
	v_or_b32_e32 v58, v49, v51
	v_fmaak_f32 v41, v30, v48, 0x4b400000
	v_fmaak_f32 v42, v31, v48, 0x4b400000
	v_fmaak_f32 v43, v32, v48, 0x4b400000
	v_fmaak_f32 v44, v33, v48, 0x4b400000
	v_perm_b32 v41, v42, v41, s33
	v_perm_b32 v43, v44, v43, s34
	v_or_b32_e32 v59, v41, v43
	s_waitcnt vmcnt(0)
	ds_read_b128 v[18:21], v38 offset:4096
	ds_read_b128 v[22:25], v38 offset:5120
	ds_read_b128 v[26:29], v38 offset:6144
	ds_read_b128 v[30:33], v38 offset:7168
	s_waitcnt lgkmcnt(0)
	s_mov_b32 m0, s35
	s_nop 0
	global_load_lds_dwordx4 v34, s[16:17] nt
	global_load_lds_dwordx4 v34, s[16:17] offset:1024 nt
	global_load_lds_dwordx4 v34, s[16:17] offset:2048 nt
	global_load_lds_dwordx4 v35, s[16:17] offset:3072 nt
	s_add_u32 s16, s16, 0x7d00
	s_addc_u32 s17, s17, 0
	v_cndmask_b32_e64 v30, 0, v30, s[18:19]
	v_cndmask_b32_e64 v31, 0, v31, s[18:19]
	v_cndmask_b32_e64 v32, 0, v32, s[18:19]
	v_cndmask_b32_e64 v33, 0, v33, s[18:19]
	v_max3_f32 v41, |v18|, |v19|, |v20|
	v_max3_f32 v42, |v21|, |v22|, |v23|
	v_max3_f32 v43, |v24|, |v25|, |v26|
	v_max3_f32 v44, |v27|, |v28|, |v29|
	v_max3_f32 v48, |v30|, |v31|, |v32|
	v_max3_f32 v41, v41, v42, |v33|
	v_max3_f32 v43, v43, v44, v48
	v_max_f32_e32 v41, v41, v43
	v_pk_add_f32 v[2:3], v[2:3], v[18:19]
	v_pk_add_f32 v[4:5], v[4:5], v[20:21]
	v_max_f32_dpp v41, v41, v41 quad_perm:[1,0,3,2] row_mask:0xf bank_mask:0xf
	v_pk_add_f32 v[6:7], v[6:7], v[22:23]
	v_pk_add_f32 v[8:9], v[8:9], v[24:25]
	v_max_f32_dpp v41, v41, v41 quad_perm:[2,3,0,1] row_mask:0xf bank_mask:0xf
	v_pk_add_f32 v[10:11], v[10:11], v[26:27]
	v_pk_add_f32 v[12:13], v[12:13], v[28:29]
	v_max_f32_dpp v41, v41, v41 row_half_mirror row_mask:0xf bank_mask:0xf
	v_pk_add_f32 v[14:15], v[14:15], v[30:31]
	v_pk_add_f32 v[16:17], v[16:17], v[32:33]
	v_max_f32_dpp v41, v41, v41 row_mirror row_mask:0xf bank_mask:0xf
	s_nop 1
	v_max_f32_dpp v41, v41, v41 row_bcast:15 row_mask:0xa bank_mask:0xf
	s_nop 1
	v_max_f32_dpp v41, v41, v41 row_bcast:31 row_mask:0xc bank_mask:0xf
	s_nop 1
	v_readlane_b32 s28, v41, 63
	s_nop 1
	v_div_scale_f32 v48, s[30:31], s28, s28, v47
	v_rcp_f32_e32 v49, v48
	s_nop 0
	v_fma_f32 v50, -v48, v49, 1.0
	v_fmac_f32_e32 v49, v50, v49
	v_mov_b32_e32 v50, s28
	v_div_scale_f32 v50, vcc, s32, v50, s32
	v_mul_f32_e32 v51, v50, v49
	v_fma_f32 v52, -v48, v51, v50
	v_fmac_f32_e32 v51, v52, v49
	v_fma_f32 v48, -v48, v51, v50
	v_div_fmas_f32 v48, v48, v49, v51
	v_div_fixup_f32 v48, v48, s28, v47
	v_cmp_gt_f32_e64 vcc, s28, 0
	v_writelane_b32 v40, s28, 1
	s_nop 0
	v_cndmask_b32_e32 v48, 0, v48, vcc
	v_fmaak_f32 v49, v18, v48, 0x4b400000
	v_fmaak_f32 v50, v19, v48, 0x4b400000
	v_fmaak_f32 v51, v20, v48, 0x4b400000
	v_fmaak_f32 v52, v21, v48, 0x4b400000
	v_perm_b32 v49, v50, v49, s33
	v_perm_b32 v51, v52, v51, s34
	v_or_b32_e32 v60, v49, v51
	v_fmaak_f32 v41, v22, v48, 0x4b400000
	v_fmaak_f32 v42, v23, v48, 0x4b400000
	v_fmaak_f32 v43, v24, v48, 0x4b400000
	v_fmaak_f32 v44, v25, v48, 0x4b400000
	v_perm_b32 v41, v42, v41, s33
	v_perm_b32 v43, v44, v43, s34
	v_or_b32_e32 v61, v41, v43
	v_fmaak_f32 v49, v26, v48, 0x4b400000
	v_fmaak_f32 v50, v27, v48, 0x4b400000
	v_fmaak_f32 v51, v28, v48, 0x4b400000
	v_fmaak_f32 v52, v29, v48, 0x4b400000
	v_perm_b32 v49, v50, v49, s33
	v_perm_b32 v51, v52, v51, s34
	v_or_b32_e32 v62, v49, v51
	v_fmaak_f32 v41, v30, v48, 0x4b400000
	v_fmaak_f32 v42, v31, v48, 0x4b400000
	v_fmaak_f32 v43, v32, v48, 0x4b400000
	v_fmaak_f32 v44, v33, v48, 0x4b400000
	v_perm_b32 v41, v42, v41, s33
	v_perm_b32 v43, v44, v43, s34
	v_or_b32_e32 v63, v41, v43
	s_waitcnt vmcnt(0)
	ds_read_b128 v[18:21], v38 offset:0
	ds_read_b128 v[22:25], v38 offset:1024
	ds_read_b128 v[26:29], v38 offset:2048
	ds_read_b128 v[30:33], v38 offset:3072
	s_waitcnt lgkmcnt(0)
	s_mov_b32 m0, s36
	s_nop 0
	global_load_lds_dwordx4 v34, s[16:17] nt
	global_load_lds_dwordx4 v34, s[16:17] offset:1024 nt
	global_load_lds_dwordx4 v34, s[16:17] offset:2048 nt
	global_load_lds_dwordx4 v35, s[16:17] offset:3072 nt
	s_add_u32 s16, s16, 0x7d00
	s_addc_u32 s17, s17, 0
	v_cndmask_b32_e64 v30, 0, v30, s[18:19]
	v_cndmask_b32_e64 v31, 0, v31, s[18:19]
	v_cndmask_b32_e64 v32, 0, v32, s[18:19]
	v_cndmask_b32_e64 v33, 0, v33, s[18:19]
	v_max3_f32 v41, |v18|, |v19|, |v20|
	v_max3_f32 v42, |v21|, |v22|, |v23|
	v_max3_f32 v43, |v24|, |v25|, |v26|
	v_max3_f32 v44, |v27|, |v28|, |v29|
	v_max3_f32 v48, |v30|, |v31|, |v32|
	v_max3_f32 v41, v41, v42, |v33|
	v_max3_f32 v43, v43, v44, v48
	v_max_f32_e32 v41, v41, v43
	v_pk_add_f32 v[2:3], v[2:3], v[18:19]
	v_pk_add_f32 v[4:5], v[4:5], v[20:21]
	v_max_f32_dpp v41, v41, v41 quad_perm:[1,0,3,2] row_mask:0xf bank_mask:0xf
	v_pk_add_f32 v[6:7], v[6:7], v[22:23]
	v_pk_add_f32 v[8:9], v[8:9], v[24:25]
	v_max_f32_dpp v41, v41, v41 quad_perm:[2,3,0,1] row_mask:0xf bank_mask:0xf
	v_pk_add_f32 v[10:11], v[10:11], v[26:27]
	v_pk_add_f32 v[12:13], v[12:13], v[28:29]
	v_max_f32_dpp v41, v41, v41 row_half_mirror row_mask:0xf bank_mask:0xf
	v_pk_add_f32 v[14:15], v[14:15], v[30:31]
	v_pk_add_f32 v[16:17], v[16:17], v[32:33]
	v_max_f32_dpp v41, v41, v41 row_mirror row_mask:0xf bank_mask:0xf
	s_nop 1
	v_max_f32_dpp v41, v41, v41 row_bcast:15 row_mask:0xa bank_mask:0xf
	s_nop 1
	v_max_f32_dpp v41, v41, v41 row_bcast:31 row_mask:0xc bank_mask:0xf
	s_nop 1
	v_readlane_b32 s28, v41, 63
	s_nop 1
	v_div_scale_f32 v48, s[30:31], s28, s28, v47
	v_rcp_f32_e32 v49, v48
	s_nop 0
	v_fma_f32 v50, -v48, v49, 1.0
	v_fmac_f32_e32 v49, v50, v49
	v_mov_b32_e32 v50, s28
	v_div_scale_f32 v50, vcc, s32, v50, s32
	v_mul_f32_e32 v51, v50, v49
	v_fma_f32 v52, -v48, v51, v50
	v_fmac_f32_e32 v51, v52, v49
	v_fma_f32 v48, -v48, v51, v50
	v_div_fmas_f32 v48, v48, v49, v51
	v_div_fixup_f32 v48, v48, s28, v47
	v_cmp_gt_f32_e64 vcc, s28, 0
	v_writelane_b32 v40, s28, 2
	s_nop 0
	v_cndmask_b32_e32 v48, 0, v48, vcc
	v_fmaak_f32 v49, v18, v48, 0x4b400000
	v_fmaak_f32 v50, v19, v48, 0x4b400000
	v_fmaak_f32 v51, v20, v48, 0x4b400000
	v_fmaak_f32 v52, v21, v48, 0x4b400000
	v_perm_b32 v49, v50, v49, s33
	v_perm_b32 v51, v52, v51, s34
	v_or_b32_e32 v64, v49, v51
	v_fmaak_f32 v41, v22, v48, 0x4b400000
	v_fmaak_f32 v42, v23, v48, 0x4b400000
	v_fmaak_f32 v43, v24, v48, 0x4b400000
	v_fmaak_f32 v44, v25, v48, 0x4b400000
	v_perm_b32 v41, v42, v41, s33
	v_perm_b32 v43, v44, v43, s34
	v_or_b32_e32 v65, v41, v43
	v_fmaak_f32 v49, v26, v48, 0x4b400000
	v_fmaak_f32 v50, v27, v48, 0x4b400000
	v_fmaak_f32 v51, v28, v48, 0x4b400000
	v_fmaak_f32 v52, v29, v48, 0x4b400000
	v_perm_b32 v49, v50, v49, s33
	v_perm_b32 v51, v52, v51, s34
	v_or_b32_e32 v66, v49, v51
	v_fmaak_f32 v41, v30, v48, 0x4b400000
	v_fmaak_f32 v42, v31, v48, 0x4b400000
	v_fmaak_f32 v43, v32, v48, 0x4b400000
	v_fmaak_f32 v44, v33, v48, 0x4b400000
	v_perm_b32 v41, v42, v41, s33
	v_perm_b32 v43, v44, v43, s34
	v_or_b32_e32 v67, v41, v43
	s_waitcnt vmcnt(0)
	ds_read_b128 v[18:21], v38 offset:4096
	ds_read_b128 v[22:25], v38 offset:5120
	ds_read_b128 v[26:29], v38 offset:6144
	ds_read_b128 v[30:33], v38 offset:7168
	s_waitcnt lgkmcnt(0)
	s_mov_b32 m0, s35
	s_nop 0
	global_load_lds_dwordx4 v34, s[16:17] nt
	global_load_lds_dwordx4 v34, s[16:17] offset:1024 nt
	global_load_lds_dwordx4 v34, s[16:17] offset:2048 nt
	global_load_lds_dwordx4 v35, s[16:17] offset:3072 nt
	s_add_u32 s16, s16, 0x7d00
	s_addc_u32 s17, s17, 0
	v_cndmask_b32_e64 v30, 0, v30, s[18:19]
	v_cndmask_b32_e64 v31, 0, v31, s[18:19]
	v_cndmask_b32_e64 v32, 0, v32, s[18:19]
	v_cndmask_b32_e64 v33, 0, v33, s[18:19]
	v_max3_f32 v41, |v18|, |v19|, |v20|
	v_max3_f32 v42, |v21|, |v22|, |v23|
	v_max3_f32 v43, |v24|, |v25|, |v26|
	v_max3_f32 v44, |v27|, |v28|, |v29|
	v_max3_f32 v48, |v30|, |v31|, |v32|
	v_max3_f32 v41, v41, v42, |v33|
	v_max3_f32 v43, v43, v44, v48
	v_max_f32_e32 v41, v41, v43
	v_pk_add_f32 v[2:3], v[2:3], v[18:19]
	v_pk_add_f32 v[4:5], v[4:5], v[20:21]
	v_max_f32_dpp v41, v41, v41 quad_perm:[1,0,3,2] row_mask:0xf bank_mask:0xf
	v_pk_add_f32 v[6:7], v[6:7], v[22:23]
	v_pk_add_f32 v[8:9], v[8:9], v[24:25]
	v_max_f32_dpp v41, v41, v41 quad_perm:[2,3,0,1] row_mask:0xf bank_mask:0xf
	v_pk_add_f32 v[10:11], v[10:11], v[26:27]
	v_pk_add_f32 v[12:13], v[12:13], v[28:29]
	v_max_f32_dpp v41, v41, v41 row_half_mirror row_mask:0xf bank_mask:0xf
	v_pk_add_f32 v[14:15], v[14:15], v[30:31]
	v_pk_add_f32 v[16:17], v[16:17], v[32:33]
	v_max_f32_dpp v41, v41, v41 row_mirror row_mask:0xf bank_mask:0xf
	s_nop 1
	v_max_f32_dpp v41, v41, v41 row_bcast:15 row_mask:0xa bank_mask:0xf
	s_nop 1
	v_max_f32_dpp v41, v41, v41 row_bcast:31 row_mask:0xc bank_mask:0xf
	s_nop 1
	v_readlane_b32 s28, v41, 63
	s_nop 1
	v_div_scale_f32 v48, s[30:31], s28, s28, v47
	v_rcp_f32_e32 v49, v48
	s_nop 0
	v_fma_f32 v50, -v48, v49, 1.0
	v_fmac_f32_e32 v49, v50, v49
	v_mov_b32_e32 v50, s28
	v_div_scale_f32 v50, vcc, s32, v50, s32
	v_mul_f32_e32 v51, v50, v49
	v_fma_f32 v52, -v48, v51, v50
	v_fmac_f32_e32 v51, v52, v49
	v_fma_f32 v48, -v48, v51, v50
	v_div_fmas_f32 v48, v48, v49, v51
	v_div_fixup_f32 v48, v48, s28, v47
	v_cmp_gt_f32_e64 vcc, s28, 0
	v_writelane_b32 v40, s28, 3
	s_nop 0
	v_cndmask_b32_e32 v48, 0, v48, vcc
	v_fmaak_f32 v49, v18, v48, 0x4b400000
	v_fmaak_f32 v50, v19, v48, 0x4b400000
	v_fmaak_f32 v51, v20, v48, 0x4b400000
	v_fmaak_f32 v52, v21, v48, 0x4b400000
	v_perm_b32 v49, v50, v49, s33
	v_perm_b32 v51, v52, v51, s34
	v_or_b32_e32 v68, v49, v51
	v_fmaak_f32 v41, v22, v48, 0x4b400000
	v_fmaak_f32 v42, v23, v48, 0x4b400000
	v_fmaak_f32 v43, v24, v48, 0x4b400000
	v_fmaak_f32 v44, v25, v48, 0x4b400000
	v_perm_b32 v41, v42, v41, s33
	v_perm_b32 v43, v44, v43, s34
	v_or_b32_e32 v69, v41, v43
	v_fmaak_f32 v49, v26, v48, 0x4b400000
	v_fmaak_f32 v50, v27, v48, 0x4b400000
	v_fmaak_f32 v51, v28, v48, 0x4b400000
	v_fmaak_f32 v52, v29, v48, 0x4b400000
	v_perm_b32 v49, v50, v49, s33
	v_perm_b32 v51, v52, v51, s34
	v_or_b32_e32 v70, v49, v51
	v_fmaak_f32 v41, v30, v48, 0x4b400000
	v_fmaak_f32 v42, v31, v48, 0x4b400000
	v_fmaak_f32 v43, v32, v48, 0x4b400000
	v_fmaak_f32 v44, v33, v48, 0x4b400000
	v_perm_b32 v41, v42, v41, s33
	v_perm_b32 v43, v44, v43, s34
	v_or_b32_e32 v71, v41, v43
	s_waitcnt vmcnt(0)
	ds_read_b128 v[18:21], v38 offset:0
	ds_read_b128 v[22:25], v38 offset:1024
	ds_read_b128 v[26:29], v38 offset:2048
	ds_read_b128 v[30:33], v38 offset:3072
	s_waitcnt lgkmcnt(0)
	s_mov_b32 m0, s36
	s_nop 0
	global_load_lds_dwordx4 v34, s[16:17] nt
	global_load_lds_dwordx4 v34, s[16:17] offset:1024 nt
	global_load_lds_dwordx4 v34, s[16:17] offset:2048 nt
	global_load_lds_dwordx4 v35, s[16:17] offset:3072 nt
	s_add_u32 s16, s16, 0x7d00
	s_addc_u32 s17, s17, 0
	v_cndmask_b32_e64 v30, 0, v30, s[18:19]
	v_cndmask_b32_e64 v31, 0, v31, s[18:19]
	v_cndmask_b32_e64 v32, 0, v32, s[18:19]
	v_cndmask_b32_e64 v33, 0, v33, s[18:19]
	v_max3_f32 v41, |v18|, |v19|, |v20|
	v_max3_f32 v42, |v21|, |v22|, |v23|
	v_max3_f32 v43, |v24|, |v25|, |v26|
	v_max3_f32 v44, |v27|, |v28|, |v29|
	v_max3_f32 v48, |v30|, |v31|, |v32|
	v_max3_f32 v41, v41, v42, |v33|
	v_max3_f32 v43, v43, v44, v48
	v_max_f32_e32 v41, v41, v43
	v_pk_add_f32 v[2:3], v[2:3], v[18:19]
	v_pk_add_f32 v[4:5], v[4:5], v[20:21]
	v_max_f32_dpp v41, v41, v41 quad_perm:[1,0,3,2] row_mask:0xf bank_mask:0xf
	v_pk_add_f32 v[6:7], v[6:7], v[22:23]
	v_pk_add_f32 v[8:9], v[8:9], v[24:25]
	v_max_f32_dpp v41, v41, v41 quad_perm:[2,3,0,1] row_mask:0xf bank_mask:0xf
	v_pk_add_f32 v[10:11], v[10:11], v[26:27]
	v_pk_add_f32 v[12:13], v[12:13], v[28:29]
	v_max_f32_dpp v41, v41, v41 row_half_mirror row_mask:0xf bank_mask:0xf
	v_pk_add_f32 v[14:15], v[14:15], v[30:31]
	v_pk_add_f32 v[16:17], v[16:17], v[32:33]
	v_max_f32_dpp v41, v41, v41 row_mirror row_mask:0xf bank_mask:0xf
	s_nop 1
	v_max_f32_dpp v41, v41, v41 row_bcast:15 row_mask:0xa bank_mask:0xf
	s_nop 1
	v_max_f32_dpp v41, v41, v41 row_bcast:31 row_mask:0xc bank_mask:0xf
	s_nop 1
	v_readlane_b32 s28, v41, 63
	s_nop 1
	v_div_scale_f32 v48, s[30:31], s28, s28, v47
	v_rcp_f32_e32 v49, v48
	s_nop 0
	v_fma_f32 v50, -v48, v49, 1.0
	v_fmac_f32_e32 v49, v50, v49
	v_mov_b32_e32 v50, s28
	v_div_scale_f32 v50, vcc, s32, v50, s32
	v_mul_f32_e32 v51, v50, v49
	v_fma_f32 v52, -v48, v51, v50
	v_fmac_f32_e32 v51, v52, v49
	v_fma_f32 v48, -v48, v51, v50
	v_div_fmas_f32 v48, v48, v49, v51
	v_div_fixup_f32 v48, v48, s28, v47
	v_cmp_gt_f32_e64 vcc, s28, 0
	v_writelane_b32 v40, s28, 4
	s_nop 0
	v_cndmask_b32_e32 v48, 0, v48, vcc
	v_fmaak_f32 v49, v18, v48, 0x4b400000
	v_fmaak_f32 v50, v19, v48, 0x4b400000
	v_fmaak_f32 v51, v20, v48, 0x4b400000
	v_fmaak_f32 v52, v21, v48, 0x4b400000
	v_perm_b32 v49, v50, v49, s33
	v_perm_b32 v51, v52, v51, s34
	v_or_b32_e32 v72, v49, v51
	v_fmaak_f32 v41, v22, v48, 0x4b400000
	v_fmaak_f32 v42, v23, v48, 0x4b400000
	v_fmaak_f32 v43, v24, v48, 0x4b400000
	v_fmaak_f32 v44, v25, v48, 0x4b400000
	v_perm_b32 v41, v42, v41, s33
	v_perm_b32 v43, v44, v43, s34
	v_or_b32_e32 v73, v41, v43
	v_fmaak_f32 v49, v26, v48, 0x4b400000
	v_fmaak_f32 v50, v27, v48, 0x4b400000
	v_fmaak_f32 v51, v28, v48, 0x4b400000
	v_fmaak_f32 v52, v29, v48, 0x4b400000
	v_perm_b32 v49, v50, v49, s33
	v_perm_b32 v51, v52, v51, s34
	v_or_b32_e32 v74, v49, v51
	v_fmaak_f32 v41, v30, v48, 0x4b400000
	v_fmaak_f32 v42, v31, v48, 0x4b400000
	v_fmaak_f32 v43, v32, v48, 0x4b400000
	v_fmaak_f32 v44, v33, v48, 0x4b400000
	v_perm_b32 v41, v42, v41, s33
	v_perm_b32 v43, v44, v43, s34
	v_or_b32_e32 v75, v41, v43
	s_waitcnt vmcnt(0)
	ds_read_b128 v[18:21], v38 offset:4096
	ds_read_b128 v[22:25], v38 offset:5120
	ds_read_b128 v[26:29], v38 offset:6144
	ds_read_b128 v[30:33], v38 offset:7168
	s_waitcnt lgkmcnt(0)
	s_mov_b32 m0, s35
	s_nop 0
	global_load_lds_dwordx4 v34, s[16:17] nt
	global_load_lds_dwordx4 v34, s[16:17] offset:1024 nt
	global_load_lds_dwordx4 v34, s[16:17] offset:2048 nt
	global_load_lds_dwordx4 v35, s[16:17] offset:3072 nt
	s_add_u32 s16, s16, 0x7d00
	s_addc_u32 s17, s17, 0
	v_cndmask_b32_e64 v30, 0, v30, s[18:19]
	v_cndmask_b32_e64 v31, 0, v31, s[18:19]
	v_cndmask_b32_e64 v32, 0, v32, s[18:19]
	v_cndmask_b32_e64 v33, 0, v33, s[18:19]
	v_max3_f32 v41, |v18|, |v19|, |v20|
	v_max3_f32 v42, |v21|, |v22|, |v23|
	v_max3_f32 v43, |v24|, |v25|, |v26|
	v_max3_f32 v44, |v27|, |v28|, |v29|
	v_max3_f32 v48, |v30|, |v31|, |v32|
	v_max3_f32 v41, v41, v42, |v33|
	v_max3_f32 v43, v43, v44, v48
	v_max_f32_e32 v41, v41, v43
	v_pk_add_f32 v[2:3], v[2:3], v[18:19]
	v_pk_add_f32 v[4:5], v[4:5], v[20:21]
	v_max_f32_dpp v41, v41, v41 quad_perm:[1,0,3,2] row_mask:0xf bank_mask:0xf
	v_pk_add_f32 v[6:7], v[6:7], v[22:23]
	v_pk_add_f32 v[8:9], v[8:9], v[24:25]
	v_max_f32_dpp v41, v41, v41 quad_perm:[2,3,0,1] row_mask:0xf bank_mask:0xf
	v_pk_add_f32 v[10:11], v[10:11], v[26:27]
	v_pk_add_f32 v[12:13], v[12:13], v[28:29]
	v_max_f32_dpp v41, v41, v41 row_half_mirror row_mask:0xf bank_mask:0xf
	v_pk_add_f32 v[14:15], v[14:15], v[30:31]
	v_pk_add_f32 v[16:17], v[16:17], v[32:33]
	v_max_f32_dpp v41, v41, v41 row_mirror row_mask:0xf bank_mask:0xf
	s_nop 1
	v_max_f32_dpp v41, v41, v41 row_bcast:15 row_mask:0xa bank_mask:0xf
	s_nop 1
	v_max_f32_dpp v41, v41, v41 row_bcast:31 row_mask:0xc bank_mask:0xf
	s_nop 1
	v_readlane_b32 s28, v41, 63
	s_nop 1
	v_div_scale_f32 v48, s[30:31], s28, s28, v47
	v_rcp_f32_e32 v49, v48
	s_nop 0
	v_fma_f32 v50, -v48, v49, 1.0
	v_fmac_f32_e32 v49, v50, v49
	v_mov_b32_e32 v50, s28
	v_div_scale_f32 v50, vcc, s32, v50, s32
	v_mul_f32_e32 v51, v50, v49
	v_fma_f32 v52, -v48, v51, v50
	v_fmac_f32_e32 v51, v52, v49
	v_fma_f32 v48, -v48, v51, v50
	v_div_fmas_f32 v48, v48, v49, v51
	v_div_fixup_f32 v48, v48, s28, v47
	v_cmp_gt_f32_e64 vcc, s28, 0
	v_writelane_b32 v40, s28, 5
	s_nop 0
	v_cndmask_b32_e32 v48, 0, v48, vcc
	v_fmaak_f32 v49, v18, v48, 0x4b400000
	v_fmaak_f32 v50, v19, v48, 0x4b400000
	v_fmaak_f32 v51, v20, v48, 0x4b400000
	v_fmaak_f32 v52, v21, v48, 0x4b400000
	v_perm_b32 v49, v50, v49, s33
	v_perm_b32 v51, v52, v51, s34
	v_or_b32_e32 v76, v49, v51
	v_fmaak_f32 v41, v22, v48, 0x4b400000
	v_fmaak_f32 v42, v23, v48, 0x4b400000
	v_fmaak_f32 v43, v24, v48, 0x4b400000
	v_fmaak_f32 v44, v25, v48, 0x4b400000
	v_perm_b32 v41, v42, v41, s33
	v_perm_b32 v43, v44, v43, s34
	v_or_b32_e32 v77, v41, v43
	v_fmaak_f32 v49, v26, v48, 0x4b400000
	v_fmaak_f32 v50, v27, v48, 0x4b400000
	v_fmaak_f32 v51, v28, v48, 0x4b400000
	v_fmaak_f32 v52, v29, v48, 0x4b400000
	v_perm_b32 v49, v50, v49, s33
	v_perm_b32 v51, v52, v51, s34
	v_or_b32_e32 v78, v49, v51
	v_fmaak_f32 v41, v30, v48, 0x4b400000
	v_fmaak_f32 v42, v31, v48, 0x4b400000
	v_fmaak_f32 v43, v32, v48, 0x4b400000
	v_fmaak_f32 v44, v33, v48, 0x4b400000
	v_perm_b32 v41, v42, v41, s33
	v_perm_b32 v43, v44, v43, s34
	v_or_b32_e32 v79, v41, v43
	s_waitcnt vmcnt(0)
	ds_read_b128 v[18:21], v38 offset:0
	ds_read_b128 v[22:25], v38 offset:1024
	ds_read_b128 v[26:29], v38 offset:2048
	ds_read_b128 v[30:33], v38 offset:3072
	s_waitcnt lgkmcnt(0)
	s_mov_b32 m0, s36
	s_nop 0
	global_load_lds_dwordx4 v34, s[16:17] nt
	global_load_lds_dwordx4 v34, s[16:17] offset:1024 nt
	global_load_lds_dwordx4 v34, s[16:17] offset:2048 nt
	global_load_lds_dwordx4 v35, s[16:17] offset:3072 nt
	s_add_u32 s16, s16, 0x7d00
	s_addc_u32 s17, s17, 0
	v_cndmask_b32_e64 v30, 0, v30, s[18:19]
	v_cndmask_b32_e64 v31, 0, v31, s[18:19]
	v_cndmask_b32_e64 v32, 0, v32, s[18:19]
	v_cndmask_b32_e64 v33, 0, v33, s[18:19]
	v_max3_f32 v41, |v18|, |v19|, |v20|
	v_max3_f32 v42, |v21|, |v22|, |v23|
	v_max3_f32 v43, |v24|, |v25|, |v26|
	v_max3_f32 v44, |v27|, |v28|, |v29|
	v_max3_f32 v48, |v30|, |v31|, |v32|
	v_max3_f32 v41, v41, v42, |v33|
	v_max3_f32 v43, v43, v44, v48
	v_max_f32_e32 v41, v41, v43
	v_pk_add_f32 v[2:3], v[2:3], v[18:19]
	v_pk_add_f32 v[4:5], v[4:5], v[20:21]
	v_max_f32_dpp v41, v41, v41 quad_perm:[1,0,3,2] row_mask:0xf bank_mask:0xf
	v_pk_add_f32 v[6:7], v[6:7], v[22:23]
	v_pk_add_f32 v[8:9], v[8:9], v[24:25]
	v_max_f32_dpp v41, v41, v41 quad_perm:[2,3,0,1] row_mask:0xf bank_mask:0xf
	v_pk_add_f32 v[10:11], v[10:11], v[26:27]
	v_pk_add_f32 v[12:13], v[12:13], v[28:29]
	v_max_f32_dpp v41, v41, v41 row_half_mirror row_mask:0xf bank_mask:0xf
	v_pk_add_f32 v[14:15], v[14:15], v[30:31]
	v_pk_add_f32 v[16:17], v[16:17], v[32:33]
	v_max_f32_dpp v41, v41, v41 row_mirror row_mask:0xf bank_mask:0xf
	s_nop 1
	v_max_f32_dpp v41, v41, v41 row_bcast:15 row_mask:0xa bank_mask:0xf
	s_nop 1
	v_max_f32_dpp v41, v41, v41 row_bcast:31 row_mask:0xc bank_mask:0xf
	s_nop 1
	v_readlane_b32 s28, v41, 63
	s_nop 1
	v_div_scale_f32 v48, s[30:31], s28, s28, v47
	v_rcp_f32_e32 v49, v48
	s_nop 0
	v_fma_f32 v50, -v48, v49, 1.0
	v_fmac_f32_e32 v49, v50, v49
	v_mov_b32_e32 v50, s28
	v_div_scale_f32 v50, vcc, s32, v50, s32
	v_mul_f32_e32 v51, v50, v49
	v_fma_f32 v52, -v48, v51, v50
	v_fmac_f32_e32 v51, v52, v49
	v_fma_f32 v48, -v48, v51, v50
	v_div_fmas_f32 v48, v48, v49, v51
	v_div_fixup_f32 v48, v48, s28, v47
	v_cmp_gt_f32_e64 vcc, s28, 0
	v_writelane_b32 v40, s28, 6
	s_nop 0
	v_cndmask_b32_e32 v48, 0, v48, vcc
	v_fmaak_f32 v49, v18, v48, 0x4b400000
	v_fmaak_f32 v50, v19, v48, 0x4b400000
	v_fmaak_f32 v51, v20, v48, 0x4b400000
	v_fmaak_f32 v52, v21, v48, 0x4b400000
	v_perm_b32 v49, v50, v49, s33
	v_perm_b32 v51, v52, v51, s34
	v_or_b32_e32 v80, v49, v51
	v_fmaak_f32 v41, v22, v48, 0x4b400000
	v_fmaak_f32 v42, v23, v48, 0x4b400000
	v_fmaak_f32 v43, v24, v48, 0x4b400000
	v_fmaak_f32 v44, v25, v48, 0x4b400000
	v_perm_b32 v41, v42, v41, s33
	v_perm_b32 v43, v44, v43, s34
	v_or_b32_e32 v81, v41, v43
	v_fmaak_f32 v49, v26, v48, 0x4b400000
	v_fmaak_f32 v50, v27, v48, 0x4b400000
	v_fmaak_f32 v51, v28, v48, 0x4b400000
	v_fmaak_f32 v52, v29, v48, 0x4b400000
	v_perm_b32 v49, v50, v49, s33
	v_perm_b32 v51, v52, v51, s34
	v_or_b32_e32 v82, v49, v51
	v_fmaak_f32 v41, v30, v48, 0x4b400000
	v_fmaak_f32 v42, v31, v48, 0x4b400000
	v_fmaak_f32 v43, v32, v48, 0x4b400000
	v_fmaak_f32 v44, v33, v48, 0x4b400000
	v_perm_b32 v41, v42, v41, s33
	v_perm_b32 v43, v44, v43, s34
	v_or_b32_e32 v83, v41, v43
	s_waitcnt vmcnt(0)
	ds_read_b128 v[18:21], v38 offset:4096
	ds_read_b128 v[22:25], v38 offset:5120
	ds_read_b128 v[26:29], v38 offset:6144
	ds_read_b128 v[30:33], v38 offset:7168
	s_waitcnt lgkmcnt(0)
	s_mov_b32 m0, s35
	s_nop 0
	global_load_lds_dwordx4 v34, s[16:17] nt
	global_load_lds_dwordx4 v34, s[16:17] offset:1024 nt
	global_load_lds_dwordx4 v34, s[16:17] offset:2048 nt
	global_load_lds_dwordx4 v35, s[16:17] offset:3072 nt
	s_add_u32 s16, s16, 0x7d00
	s_addc_u32 s17, s17, 0
	v_cndmask_b32_e64 v30, 0, v30, s[18:19]
	v_cndmask_b32_e64 v31, 0, v31, s[18:19]
	v_cndmask_b32_e64 v32, 0, v32, s[18:19]
	v_cndmask_b32_e64 v33, 0, v33, s[18:19]
	v_max3_f32 v41, |v18|, |v19|, |v20|
	v_max3_f32 v42, |v21|, |v22|, |v23|
	v_max3_f32 v43, |v24|, |v25|, |v26|
	v_max3_f32 v44, |v27|, |v28|, |v29|
	v_max3_f32 v48, |v30|, |v31|, |v32|
	v_max3_f32 v41, v41, v42, |v33|
	v_max3_f32 v43, v43, v44, v48
	v_max_f32_e32 v41, v41, v43
	v_pk_add_f32 v[2:3], v[2:3], v[18:19]
	v_pk_add_f32 v[4:5], v[4:5], v[20:21]
	v_max_f32_dpp v41, v41, v41 quad_perm:[1,0,3,2] row_mask:0xf bank_mask:0xf
	v_pk_add_f32 v[6:7], v[6:7], v[22:23]
	v_pk_add_f32 v[8:9], v[8:9], v[24:25]
	v_max_f32_dpp v41, v41, v41 quad_perm:[2,3,0,1] row_mask:0xf bank_mask:0xf
	v_pk_add_f32 v[10:11], v[10:11], v[26:27]
	v_pk_add_f32 v[12:13], v[12:13], v[28:29]
	v_max_f32_dpp v41, v41, v41 row_half_mirror row_mask:0xf bank_mask:0xf
	v_pk_add_f32 v[14:15], v[14:15], v[30:31]
	v_pk_add_f32 v[16:17], v[16:17], v[32:33]
	v_max_f32_dpp v41, v41, v41 row_mirror row_mask:0xf bank_mask:0xf
	s_nop 1
	v_max_f32_dpp v41, v41, v41 row_bcast:15 row_mask:0xa bank_mask:0xf
	s_nop 1
	v_max_f32_dpp v41, v41, v41 row_bcast:31 row_mask:0xc bank_mask:0xf
	s_nop 1
	v_readlane_b32 s28, v41, 63
	s_nop 1
	v_div_scale_f32 v48, s[30:31], s28, s28, v47
	v_rcp_f32_e32 v49, v48
	s_nop 0
	v_fma_f32 v50, -v48, v49, 1.0
	v_fmac_f32_e32 v49, v50, v49
	v_mov_b32_e32 v50, s28
	v_div_scale_f32 v50, vcc, s32, v50, s32
	v_mul_f32_e32 v51, v50, v49
	v_fma_f32 v52, -v48, v51, v50
	v_fmac_f32_e32 v51, v52, v49
	v_fma_f32 v48, -v48, v51, v50
	v_div_fmas_f32 v48, v48, v49, v51
	v_div_fixup_f32 v48, v48, s28, v47
	v_cmp_gt_f32_e64 vcc, s28, 0
	v_writelane_b32 v40, s28, 7
	s_nop 0
	v_cndmask_b32_e32 v48, 0, v48, vcc
	v_fmaak_f32 v49, v18, v48, 0x4b400000
	v_fmaak_f32 v50, v19, v48, 0x4b400000
	v_fmaak_f32 v51, v20, v48, 0x4b400000
	v_fmaak_f32 v52, v21, v48, 0x4b400000
	v_perm_b32 v49, v50, v49, s33
	v_perm_b32 v51, v52, v51, s34
	v_or_b32_e32 v84, v49, v51
	v_fmaak_f32 v41, v22, v48, 0x4b400000
	v_fmaak_f32 v42, v23, v48, 0x4b400000
	v_fmaak_f32 v43, v24, v48, 0x4b400000
	v_fmaak_f32 v44, v25, v48, 0x4b400000
	v_perm_b32 v41, v42, v41, s33
	v_perm_b32 v43, v44, v43, s34
	v_or_b32_e32 v85, v41, v43
	v_fmaak_f32 v49, v26, v48, 0x4b400000
	v_fmaak_f32 v50, v27, v48, 0x4b400000
	v_fmaak_f32 v51, v28, v48, 0x4b400000
	v_fmaak_f32 v52, v29, v48, 0x4b400000
	v_perm_b32 v49, v50, v49, s33
	v_perm_b32 v51, v52, v51, s34
	v_or_b32_e32 v86, v49, v51
	v_fmaak_f32 v41, v30, v48, 0x4b400000
	v_fmaak_f32 v42, v31, v48, 0x4b400000
	v_fmaak_f32 v43, v32, v48, 0x4b400000
	v_fmaak_f32 v44, v33, v48, 0x4b400000
	v_perm_b32 v41, v42, v41, s33
	v_perm_b32 v43, v44, v43, s34
	v_or_b32_e32 v87, v41, v43
	s_waitcnt vmcnt(0)
	ds_read_b128 v[18:21], v38 offset:0
	ds_read_b128 v[22:25], v38 offset:1024
	ds_read_b128 v[26:29], v38 offset:2048
	ds_read_b128 v[30:33], v38 offset:3072
	s_waitcnt lgkmcnt(0)
	s_mov_b32 m0, s36
	s_nop 0
	global_load_lds_dwordx4 v34, s[16:17] nt
	global_load_lds_dwordx4 v34, s[16:17] offset:1024 nt
	global_load_lds_dwordx4 v34, s[16:17] offset:2048 nt
	global_load_lds_dwordx4 v35, s[16:17] offset:3072 nt
	s_add_u32 s16, s16, 0x7d00
	s_addc_u32 s17, s17, 0
	v_cndmask_b32_e64 v30, 0, v30, s[18:19]
	v_cndmask_b32_e64 v31, 0, v31, s[18:19]
	v_cndmask_b32_e64 v32, 0, v32, s[18:19]
	v_cndmask_b32_e64 v33, 0, v33, s[18:19]
	v_max3_f32 v41, |v18|, |v19|, |v20|
	v_max3_f32 v42, |v21|, |v22|, |v23|
	v_max3_f32 v43, |v24|, |v25|, |v26|
	v_max3_f32 v44, |v27|, |v28|, |v29|
	v_max3_f32 v48, |v30|, |v31|, |v32|
	v_max3_f32 v41, v41, v42, |v33|
	v_max3_f32 v43, v43, v44, v48
	v_max_f32_e32 v41, v41, v43
	v_pk_add_f32 v[2:3], v[2:3], v[18:19]
	v_pk_add_f32 v[4:5], v[4:5], v[20:21]
	v_max_f32_dpp v41, v41, v41 quad_perm:[1,0,3,2] row_mask:0xf bank_mask:0xf
	v_pk_add_f32 v[6:7], v[6:7], v[22:23]
	v_pk_add_f32 v[8:9], v[8:9], v[24:25]
	v_max_f32_dpp v41, v41, v41 quad_perm:[2,3,0,1] row_mask:0xf bank_mask:0xf
	v_pk_add_f32 v[10:11], v[10:11], v[26:27]
	v_pk_add_f32 v[12:13], v[12:13], v[28:29]
	v_max_f32_dpp v41, v41, v41 row_half_mirror row_mask:0xf bank_mask:0xf
	v_pk_add_f32 v[14:15], v[14:15], v[30:31]
	v_pk_add_f32 v[16:17], v[16:17], v[32:33]
	v_max_f32_dpp v41, v41, v41 row_mirror row_mask:0xf bank_mask:0xf
	s_nop 1
	v_max_f32_dpp v41, v41, v41 row_bcast:15 row_mask:0xa bank_mask:0xf
	s_nop 1
	v_max_f32_dpp v41, v41, v41 row_bcast:31 row_mask:0xc bank_mask:0xf
	s_nop 1
	v_readlane_b32 s28, v41, 63
	s_nop 1
	v_div_scale_f32 v48, s[30:31], s28, s28, v47
	v_rcp_f32_e32 v49, v48
	s_nop 0
	v_fma_f32 v50, -v48, v49, 1.0
	v_fmac_f32_e32 v49, v50, v49
	v_mov_b32_e32 v50, s28
	v_div_scale_f32 v50, vcc, s32, v50, s32
	v_mul_f32_e32 v51, v50, v49
	v_fma_f32 v52, -v48, v51, v50
	v_fmac_f32_e32 v51, v52, v49
	v_fma_f32 v48, -v48, v51, v50
	v_div_fmas_f32 v48, v48, v49, v51
	v_div_fixup_f32 v48, v48, s28, v47
	v_cmp_gt_f32_e64 vcc, s28, 0
	v_writelane_b32 v40, s28, 8
	s_nop 0
	v_cndmask_b32_e32 v48, 0, v48, vcc
	v_fmaak_f32 v49, v18, v48, 0x4b400000
	v_fmaak_f32 v50, v19, v48, 0x4b400000
	v_fmaak_f32 v51, v20, v48, 0x4b400000
	v_fmaak_f32 v52, v21, v48, 0x4b400000
	v_perm_b32 v49, v50, v49, s33
	v_perm_b32 v51, v52, v51, s34
	v_or_b32_e32 v88, v49, v51
	v_fmaak_f32 v41, v22, v48, 0x4b400000
	v_fmaak_f32 v42, v23, v48, 0x4b400000
	v_fmaak_f32 v43, v24, v48, 0x4b400000
	v_fmaak_f32 v44, v25, v48, 0x4b400000
	v_perm_b32 v41, v42, v41, s33
	v_perm_b32 v43, v44, v43, s34
	v_or_b32_e32 v89, v41, v43
	v_fmaak_f32 v49, v26, v48, 0x4b400000
	v_fmaak_f32 v50, v27, v48, 0x4b400000
	v_fmaak_f32 v51, v28, v48, 0x4b400000
	v_fmaak_f32 v52, v29, v48, 0x4b400000
	v_perm_b32 v49, v50, v49, s33
	v_perm_b32 v51, v52, v51, s34
	v_or_b32_e32 v90, v49, v51
	v_fmaak_f32 v41, v30, v48, 0x4b400000
	v_fmaak_f32 v42, v31, v48, 0x4b400000
	v_fmaak_f32 v43, v32, v48, 0x4b400000
	v_fmaak_f32 v44, v33, v48, 0x4b400000
	v_perm_b32 v41, v42, v41, s33
	v_perm_b32 v43, v44, v43, s34
	v_or_b32_e32 v91, v41, v43
	s_waitcnt vmcnt(0)
	ds_read_b128 v[18:21], v38 offset:4096
	ds_read_b128 v[22:25], v38 offset:5120
	ds_read_b128 v[26:29], v38 offset:6144
	ds_read_b128 v[30:33], v38 offset:7168
	s_waitcnt lgkmcnt(0)
	s_mov_b32 m0, s35
	s_nop 0
	global_load_lds_dwordx4 v34, s[16:17] nt
	global_load_lds_dwordx4 v34, s[16:17] offset:1024 nt
	global_load_lds_dwordx4 v34, s[16:17] offset:2048 nt
	global_load_lds_dwordx4 v35, s[16:17] offset:3072 nt
	s_add_u32 s16, s16, 0x7d00
	s_addc_u32 s17, s17, 0
	v_cndmask_b32_e64 v30, 0, v30, s[18:19]
	v_cndmask_b32_e64 v31, 0, v31, s[18:19]
	v_cndmask_b32_e64 v32, 0, v32, s[18:19]
	v_cndmask_b32_e64 v33, 0, v33, s[18:19]
	v_max3_f32 v41, |v18|, |v19|, |v20|
	v_max3_f32 v42, |v21|, |v22|, |v23|
	v_max3_f32 v43, |v24|, |v25|, |v26|
	v_max3_f32 v44, |v27|, |v28|, |v29|
	v_max3_f32 v48, |v30|, |v31|, |v32|
	v_max3_f32 v41, v41, v42, |v33|
	v_max3_f32 v43, v43, v44, v48
	v_max_f32_e32 v41, v41, v43
	v_pk_add_f32 v[2:3], v[2:3], v[18:19]
	v_pk_add_f32 v[4:5], v[4:5], v[20:21]
	v_max_f32_dpp v41, v41, v41 quad_perm:[1,0,3,2] row_mask:0xf bank_mask:0xf
	v_pk_add_f32 v[6:7], v[6:7], v[22:23]
	v_pk_add_f32 v[8:9], v[8:9], v[24:25]
	v_max_f32_dpp v41, v41, v41 quad_perm:[2,3,0,1] row_mask:0xf bank_mask:0xf
	v_pk_add_f32 v[10:11], v[10:11], v[26:27]
	v_pk_add_f32 v[12:13], v[12:13], v[28:29]
	v_max_f32_dpp v41, v41, v41 row_half_mirror row_mask:0xf bank_mask:0xf
	v_pk_add_f32 v[14:15], v[14:15], v[30:31]
	v_pk_add_f32 v[16:17], v[16:17], v[32:33]
	v_max_f32_dpp v41, v41, v41 row_mirror row_mask:0xf bank_mask:0xf
	s_nop 1
	v_max_f32_dpp v41, v41, v41 row_bcast:15 row_mask:0xa bank_mask:0xf
	s_nop 1
	v_max_f32_dpp v41, v41, v41 row_bcast:31 row_mask:0xc bank_mask:0xf
	s_nop 1
	v_readlane_b32 s28, v41, 63
	s_nop 1
	v_div_scale_f32 v48, s[30:31], s28, s28, v47
	v_rcp_f32_e32 v49, v48
	s_nop 0
	v_fma_f32 v50, -v48, v49, 1.0
	v_fmac_f32_e32 v49, v50, v49
	v_mov_b32_e32 v50, s28
	v_div_scale_f32 v50, vcc, s32, v50, s32
	v_mul_f32_e32 v51, v50, v49
	v_fma_f32 v52, -v48, v51, v50
	v_fmac_f32_e32 v51, v52, v49
	v_fma_f32 v48, -v48, v51, v50
	v_div_fmas_f32 v48, v48, v49, v51
	v_div_fixup_f32 v48, v48, s28, v47
	v_cmp_gt_f32_e64 vcc, s28, 0
	v_writelane_b32 v40, s28, 9
	s_nop 0
	v_cndmask_b32_e32 v48, 0, v48, vcc
	v_fmaak_f32 v49, v18, v48, 0x4b400000
	v_fmaak_f32 v50, v19, v48, 0x4b400000
	v_fmaak_f32 v51, v20, v48, 0x4b400000
	v_fmaak_f32 v52, v21, v48, 0x4b400000
	v_perm_b32 v49, v50, v49, s33
	v_perm_b32 v51, v52, v51, s34
	v_or_b32_e32 v92, v49, v51
	v_fmaak_f32 v41, v22, v48, 0x4b400000
	v_fmaak_f32 v42, v23, v48, 0x4b400000
	v_fmaak_f32 v43, v24, v48, 0x4b400000
	v_fmaak_f32 v44, v25, v48, 0x4b400000
	v_perm_b32 v41, v42, v41, s33
	v_perm_b32 v43, v44, v43, s34
	v_or_b32_e32 v93, v41, v43
	v_fmaak_f32 v49, v26, v48, 0x4b400000
	v_fmaak_f32 v50, v27, v48, 0x4b400000
	v_fmaak_f32 v51, v28, v48, 0x4b400000
	v_fmaak_f32 v52, v29, v48, 0x4b400000
	v_perm_b32 v49, v50, v49, s33
	v_perm_b32 v51, v52, v51, s34
	v_or_b32_e32 v94, v49, v51
	v_fmaak_f32 v41, v30, v48, 0x4b400000
	v_fmaak_f32 v42, v31, v48, 0x4b400000
	v_fmaak_f32 v43, v32, v48, 0x4b400000
	v_fmaak_f32 v44, v33, v48, 0x4b400000
	v_perm_b32 v41, v42, v41, s33
	v_perm_b32 v43, v44, v43, s34
	v_or_b32_e32 v95, v41, v43
	s_waitcnt vmcnt(0)
	ds_read_b128 v[18:21], v38 offset:0
	ds_read_b128 v[22:25], v38 offset:1024
	ds_read_b128 v[26:29], v38 offset:2048
	ds_read_b128 v[30:33], v38 offset:3072
	s_waitcnt lgkmcnt(0)
	s_mov_b32 m0, s36
	s_nop 0
	global_load_lds_dwordx4 v34, s[16:17] nt
	global_load_lds_dwordx4 v34, s[16:17] offset:1024 nt
	global_load_lds_dwordx4 v34, s[16:17] offset:2048 nt
	global_load_lds_dwordx4 v35, s[16:17] offset:3072 nt
	s_add_u32 s16, s16, 0x7d00
	s_addc_u32 s17, s17, 0
	v_cndmask_b32_e64 v30, 0, v30, s[18:19]
	v_cndmask_b32_e64 v31, 0, v31, s[18:19]
	v_cndmask_b32_e64 v32, 0, v32, s[18:19]
	v_cndmask_b32_e64 v33, 0, v33, s[18:19]
	v_max3_f32 v41, |v18|, |v19|, |v20|
	v_max3_f32 v42, |v21|, |v22|, |v23|
	v_max3_f32 v43, |v24|, |v25|, |v26|
	v_max3_f32 v44, |v27|, |v28|, |v29|
	v_max3_f32 v48, |v30|, |v31|, |v32|
	v_max3_f32 v41, v41, v42, |v33|
	v_max3_f32 v43, v43, v44, v48
	v_max_f32_e32 v41, v41, v43
	v_pk_add_f32 v[2:3], v[2:3], v[18:19]
	v_pk_add_f32 v[4:5], v[4:5], v[20:21]
	v_max_f32_dpp v41, v41, v41 quad_perm:[1,0,3,2] row_mask:0xf bank_mask:0xf
	v_pk_add_f32 v[6:7], v[6:7], v[22:23]
	v_pk_add_f32 v[8:9], v[8:9], v[24:25]
	v_max_f32_dpp v41, v41, v41 quad_perm:[2,3,0,1] row_mask:0xf bank_mask:0xf
	v_pk_add_f32 v[10:11], v[10:11], v[26:27]
	v_pk_add_f32 v[12:13], v[12:13], v[28:29]
	v_max_f32_dpp v41, v41, v41 row_half_mirror row_mask:0xf bank_mask:0xf
	v_pk_add_f32 v[14:15], v[14:15], v[30:31]
	v_pk_add_f32 v[16:17], v[16:17], v[32:33]
	v_max_f32_dpp v41, v41, v41 row_mirror row_mask:0xf bank_mask:0xf
	s_nop 1
	v_max_f32_dpp v41, v41, v41 row_bcast:15 row_mask:0xa bank_mask:0xf
	s_nop 1
	v_max_f32_dpp v41, v41, v41 row_bcast:31 row_mask:0xc bank_mask:0xf
	s_nop 1
	v_readlane_b32 s28, v41, 63
	s_nop 1
	v_div_scale_f32 v48, s[30:31], s28, s28, v47
	v_rcp_f32_e32 v49, v48
	s_nop 0
	v_fma_f32 v50, -v48, v49, 1.0
	v_fmac_f32_e32 v49, v50, v49
	v_mov_b32_e32 v50, s28
	v_div_scale_f32 v50, vcc, s32, v50, s32
	v_mul_f32_e32 v51, v50, v49
	v_fma_f32 v52, -v48, v51, v50
	v_fmac_f32_e32 v51, v52, v49
	v_fma_f32 v48, -v48, v51, v50
	v_div_fmas_f32 v48, v48, v49, v51
	v_div_fixup_f32 v48, v48, s28, v47
	v_cmp_gt_f32_e64 vcc, s28, 0
	v_writelane_b32 v40, s28, 10
	s_nop 0
	v_cndmask_b32_e32 v48, 0, v48, vcc
	v_fmaak_f32 v49, v18, v48, 0x4b400000
	v_fmaak_f32 v50, v19, v48, 0x4b400000
	v_fmaak_f32 v51, v20, v48, 0x4b400000
	v_fmaak_f32 v52, v21, v48, 0x4b400000
	v_perm_b32 v49, v50, v49, s33
	v_perm_b32 v51, v52, v51, s34
	v_or_b32_e32 v96, v49, v51
	v_fmaak_f32 v41, v22, v48, 0x4b400000
	v_fmaak_f32 v42, v23, v48, 0x4b400000
	v_fmaak_f32 v43, v24, v48, 0x4b400000
	v_fmaak_f32 v44, v25, v48, 0x4b400000
	v_perm_b32 v41, v42, v41, s33
	v_perm_b32 v43, v44, v43, s34
	v_or_b32_e32 v97, v41, v43
	v_fmaak_f32 v49, v26, v48, 0x4b400000
	v_fmaak_f32 v50, v27, v48, 0x4b400000
	v_fmaak_f32 v51, v28, v48, 0x4b400000
	v_fmaak_f32 v52, v29, v48, 0x4b400000
	v_perm_b32 v49, v50, v49, s33
	v_perm_b32 v51, v52, v51, s34
	v_or_b32_e32 v98, v49, v51
	v_fmaak_f32 v41, v30, v48, 0x4b400000
	v_fmaak_f32 v42, v31, v48, 0x4b400000
	v_fmaak_f32 v43, v32, v48, 0x4b400000
	v_fmaak_f32 v44, v33, v48, 0x4b400000
	v_perm_b32 v41, v42, v41, s33
	v_perm_b32 v43, v44, v43, s34
	v_or_b32_e32 v99, v41, v43
	s_waitcnt vmcnt(0)
	ds_read_b128 v[18:21], v38 offset:4096
	ds_read_b128 v[22:25], v38 offset:5120
	ds_read_b128 v[26:29], v38 offset:6144
	ds_read_b128 v[30:33], v38 offset:7168
	s_waitcnt lgkmcnt(0)
	s_mov_b32 m0, s35
	s_nop 0
	global_load_lds_dwordx4 v34, s[16:17] nt
	global_load_lds_dwordx4 v34, s[16:17] offset:1024 nt
	global_load_lds_dwordx4 v34, s[16:17] offset:2048 nt
	global_load_lds_dwordx4 v35, s[16:17] offset:3072 nt
	s_add_u32 s16, s16, 0x7d00
	s_addc_u32 s17, s17, 0
	v_cndmask_b32_e64 v30, 0, v30, s[18:19]
	v_cndmask_b32_e64 v31, 0, v31, s[18:19]
	v_cndmask_b32_e64 v32, 0, v32, s[18:19]
	v_cndmask_b32_e64 v33, 0, v33, s[18:19]
	v_max3_f32 v41, |v18|, |v19|, |v20|
	v_max3_f32 v42, |v21|, |v22|, |v23|
	v_max3_f32 v43, |v24|, |v25|, |v26|
	v_max3_f32 v44, |v27|, |v28|, |v29|
	v_max3_f32 v48, |v30|, |v31|, |v32|
	v_max3_f32 v41, v41, v42, |v33|
	v_max3_f32 v43, v43, v44, v48
	v_max_f32_e32 v41, v41, v43
	v_pk_add_f32 v[2:3], v[2:3], v[18:19]
	v_pk_add_f32 v[4:5], v[4:5], v[20:21]
	v_max_f32_dpp v41, v41, v41 quad_perm:[1,0,3,2] row_mask:0xf bank_mask:0xf
	v_pk_add_f32 v[6:7], v[6:7], v[22:23]
	v_pk_add_f32 v[8:9], v[8:9], v[24:25]
	v_max_f32_dpp v41, v41, v41 quad_perm:[2,3,0,1] row_mask:0xf bank_mask:0xf
	v_pk_add_f32 v[10:11], v[10:11], v[26:27]
	v_pk_add_f32 v[12:13], v[12:13], v[28:29]
	v_max_f32_dpp v41, v41, v41 row_half_mirror row_mask:0xf bank_mask:0xf
	v_pk_add_f32 v[14:15], v[14:15], v[30:31]
	v_pk_add_f32 v[16:17], v[16:17], v[32:33]
	v_max_f32_dpp v41, v41, v41 row_mirror row_mask:0xf bank_mask:0xf
	s_nop 1
	v_max_f32_dpp v41, v41, v41 row_bcast:15 row_mask:0xa bank_mask:0xf
	s_nop 1
	v_max_f32_dpp v41, v41, v41 row_bcast:31 row_mask:0xc bank_mask:0xf
	s_nop 1
	v_readlane_b32 s28, v41, 63
	s_nop 1
	v_div_scale_f32 v48, s[30:31], s28, s28, v47
	v_rcp_f32_e32 v49, v48
	s_nop 0
	v_fma_f32 v50, -v48, v49, 1.0
	v_fmac_f32_e32 v49, v50, v49
	v_mov_b32_e32 v50, s28
	v_div_scale_f32 v50, vcc, s32, v50, s32
	v_mul_f32_e32 v51, v50, v49
	v_fma_f32 v52, -v48, v51, v50
	v_fmac_f32_e32 v51, v52, v49
	v_fma_f32 v48, -v48, v51, v50
	v_div_fmas_f32 v48, v48, v49, v51
	v_div_fixup_f32 v48, v48, s28, v47
	v_cmp_gt_f32_e64 vcc, s28, 0
	v_writelane_b32 v40, s28, 11
	s_nop 0
	v_cndmask_b32_e32 v48, 0, v48, vcc
	v_fmaak_f32 v49, v18, v48, 0x4b400000
	v_fmaak_f32 v50, v19, v48, 0x4b400000
	v_fmaak_f32 v51, v20, v48, 0x4b400000
	v_fmaak_f32 v52, v21, v48, 0x4b400000
	v_perm_b32 v49, v50, v49, s33
	v_perm_b32 v51, v52, v51, s34
	v_or_b32_e32 v100, v49, v51
	v_fmaak_f32 v41, v22, v48, 0x4b400000
	v_fmaak_f32 v42, v23, v48, 0x4b400000
	v_fmaak_f32 v43, v24, v48, 0x4b400000
	v_fmaak_f32 v44, v25, v48, 0x4b400000
	v_perm_b32 v41, v42, v41, s33
	v_perm_b32 v43, v44, v43, s34
	v_or_b32_e32 v101, v41, v43
	v_fmaak_f32 v49, v26, v48, 0x4b400000
	v_fmaak_f32 v50, v27, v48, 0x4b400000
	v_fmaak_f32 v51, v28, v48, 0x4b400000
	v_fmaak_f32 v52, v29, v48, 0x4b400000
	v_perm_b32 v49, v50, v49, s33
	v_perm_b32 v51, v52, v51, s34
	v_or_b32_e32 v102, v49, v51
	v_fmaak_f32 v41, v30, v48, 0x4b400000
	v_fmaak_f32 v42, v31, v48, 0x4b400000
	v_fmaak_f32 v43, v32, v48, 0x4b400000
	v_fmaak_f32 v44, v33, v48, 0x4b400000
	v_perm_b32 v41, v42, v41, s33
	v_perm_b32 v43, v44, v43, s34
	v_or_b32_e32 v103, v41, v43
	s_waitcnt vmcnt(0)
	ds_read_b128 v[18:21], v38 offset:0
	ds_read_b128 v[22:25], v38 offset:1024
	ds_read_b128 v[26:29], v38 offset:2048
	ds_read_b128 v[30:33], v38 offset:3072
	s_waitcnt lgkmcnt(0)
	s_mov_b32 m0, s36
	s_nop 0
	global_load_lds_dwordx4 v34, s[16:17] nt
	global_load_lds_dwordx4 v34, s[16:17] offset:1024 nt
	global_load_lds_dwordx4 v34, s[16:17] offset:2048 nt
	global_load_lds_dwordx4 v35, s[16:17] offset:3072 nt
	s_add_u32 s16, s16, 0x7d00
	s_addc_u32 s17, s17, 0
	v_cndmask_b32_e64 v30, 0, v30, s[18:19]
	v_cndmask_b32_e64 v31, 0, v31, s[18:19]
	v_cndmask_b32_e64 v32, 0, v32, s[18:19]
	v_cndmask_b32_e64 v33, 0, v33, s[18:19]
	v_max3_f32 v41, |v18|, |v19|, |v20|
	v_max3_f32 v42, |v21|, |v22|, |v23|
	v_max3_f32 v43, |v24|, |v25|, |v26|
	v_max3_f32 v44, |v27|, |v28|, |v29|
	v_max3_f32 v48, |v30|, |v31|, |v32|
	v_max3_f32 v41, v41, v42, |v33|
	v_max3_f32 v43, v43, v44, v48
	v_max_f32_e32 v41, v41, v43
	v_pk_add_f32 v[2:3], v[2:3], v[18:19]
	v_pk_add_f32 v[4:5], v[4:5], v[20:21]
	v_max_f32_dpp v41, v41, v41 quad_perm:[1,0,3,2] row_mask:0xf bank_mask:0xf
	v_pk_add_f32 v[6:7], v[6:7], v[22:23]
	v_pk_add_f32 v[8:9], v[8:9], v[24:25]
	v_max_f32_dpp v41, v41, v41 quad_perm:[2,3,0,1] row_mask:0xf bank_mask:0xf
	v_pk_add_f32 v[10:11], v[10:11], v[26:27]
	v_pk_add_f32 v[12:13], v[12:13], v[28:29]
	v_max_f32_dpp v41, v41, v41 row_half_mirror row_mask:0xf bank_mask:0xf
	v_pk_add_f32 v[14:15], v[14:15], v[30:31]
	v_pk_add_f32 v[16:17], v[16:17], v[32:33]
	v_max_f32_dpp v41, v41, v41 row_mirror row_mask:0xf bank_mask:0xf
	s_nop 1
	v_max_f32_dpp v41, v41, v41 row_bcast:15 row_mask:0xa bank_mask:0xf
	s_nop 1
	v_max_f32_dpp v41, v41, v41 row_bcast:31 row_mask:0xc bank_mask:0xf
	s_nop 1
	v_readlane_b32 s28, v41, 63
	s_nop 1
	v_div_scale_f32 v48, s[30:31], s28, s28, v47
	v_rcp_f32_e32 v49, v48
	s_nop 0
	v_fma_f32 v50, -v48, v49, 1.0
	v_fmac_f32_e32 v49, v50, v49
	v_mov_b32_e32 v50, s28
	v_div_scale_f32 v50, vcc, s32, v50, s32
	v_mul_f32_e32 v51, v50, v49
	v_fma_f32 v52, -v48, v51, v50
	v_fmac_f32_e32 v51, v52, v49
	v_fma_f32 v48, -v48, v51, v50
	v_div_fmas_f32 v48, v48, v49, v51
	v_div_fixup_f32 v48, v48, s28, v47
	v_cmp_gt_f32_e64 vcc, s28, 0
	v_writelane_b32 v40, s28, 12
	s_nop 0
	v_cndmask_b32_e32 v48, 0, v48, vcc
	v_fmaak_f32 v49, v18, v48, 0x4b400000
	v_fmaak_f32 v50, v19, v48, 0x4b400000
	v_fmaak_f32 v51, v20, v48, 0x4b400000
	v_fmaak_f32 v52, v21, v48, 0x4b400000
	v_perm_b32 v49, v50, v49, s33
	v_perm_b32 v51, v52, v51, s34
	v_or_b32_e32 v104, v49, v51
	v_fmaak_f32 v41, v22, v48, 0x4b400000
	v_fmaak_f32 v42, v23, v48, 0x4b400000
	v_fmaak_f32 v43, v24, v48, 0x4b400000
	v_fmaak_f32 v44, v25, v48, 0x4b400000
	v_perm_b32 v41, v42, v41, s33
	v_perm_b32 v43, v44, v43, s34
	v_or_b32_e32 v105, v41, v43
	v_fmaak_f32 v49, v26, v48, 0x4b400000
	v_fmaak_f32 v50, v27, v48, 0x4b400000
	v_fmaak_f32 v51, v28, v48, 0x4b400000
	v_fmaak_f32 v52, v29, v48, 0x4b400000
	v_perm_b32 v49, v50, v49, s33
	v_perm_b32 v51, v52, v51, s34
	v_or_b32_e32 v106, v49, v51
	v_fmaak_f32 v41, v30, v48, 0x4b400000
	v_fmaak_f32 v42, v31, v48, 0x4b400000
	v_fmaak_f32 v43, v32, v48, 0x4b400000
	v_fmaak_f32 v44, v33, v48, 0x4b400000
	v_perm_b32 v41, v42, v41, s33
	v_perm_b32 v43, v44, v43, s34
	v_or_b32_e32 v107, v41, v43
	s_waitcnt vmcnt(0)
	ds_read_b128 v[18:21], v38 offset:4096
	ds_read_b128 v[22:25], v38 offset:5120
	ds_read_b128 v[26:29], v38 offset:6144
	ds_read_b128 v[30:33], v38 offset:7168
	s_waitcnt lgkmcnt(0)
	s_mov_b32 m0, s35
	s_nop 0
	global_load_lds_dwordx4 v34, s[16:17] nt
	global_load_lds_dwordx4 v34, s[16:17] offset:1024 nt
	global_load_lds_dwordx4 v34, s[16:17] offset:2048 nt
	global_load_lds_dwordx4 v35, s[16:17] offset:3072 nt
	s_add_u32 s16, s16, 0x7d00
	s_addc_u32 s17, s17, 0
	v_cndmask_b32_e64 v30, 0, v30, s[18:19]
	v_cndmask_b32_e64 v31, 0, v31, s[18:19]
	v_cndmask_b32_e64 v32, 0, v32, s[18:19]
	v_cndmask_b32_e64 v33, 0, v33, s[18:19]
	v_max3_f32 v41, |v18|, |v19|, |v20|
	v_max3_f32 v42, |v21|, |v22|, |v23|
	v_max3_f32 v43, |v24|, |v25|, |v26|
	v_max3_f32 v44, |v27|, |v28|, |v29|
	v_max3_f32 v48, |v30|, |v31|, |v32|
	v_max3_f32 v41, v41, v42, |v33|
	v_max3_f32 v43, v43, v44, v48
	v_max_f32_e32 v41, v41, v43
	v_pk_add_f32 v[2:3], v[2:3], v[18:19]
	v_pk_add_f32 v[4:5], v[4:5], v[20:21]
	v_max_f32_dpp v41, v41, v41 quad_perm:[1,0,3,2] row_mask:0xf bank_mask:0xf
	v_pk_add_f32 v[6:7], v[6:7], v[22:23]
	v_pk_add_f32 v[8:9], v[8:9], v[24:25]
	v_max_f32_dpp v41, v41, v41 quad_perm:[2,3,0,1] row_mask:0xf bank_mask:0xf
	v_pk_add_f32 v[10:11], v[10:11], v[26:27]
	v_pk_add_f32 v[12:13], v[12:13], v[28:29]
	v_max_f32_dpp v41, v41, v41 row_half_mirror row_mask:0xf bank_mask:0xf
	v_pk_add_f32 v[14:15], v[14:15], v[30:31]
	v_pk_add_f32 v[16:17], v[16:17], v[32:33]
	v_max_f32_dpp v41, v41, v41 row_mirror row_mask:0xf bank_mask:0xf
	s_nop 1
	v_max_f32_dpp v41, v41, v41 row_bcast:15 row_mask:0xa bank_mask:0xf
	s_nop 1
	v_max_f32_dpp v41, v41, v41 row_bcast:31 row_mask:0xc bank_mask:0xf
	s_nop 1
	v_readlane_b32 s28, v41, 63
	s_nop 1
	v_div_scale_f32 v48, s[30:31], s28, s28, v47
	v_rcp_f32_e32 v49, v48
	s_nop 0
	v_fma_f32 v50, -v48, v49, 1.0
	v_fmac_f32_e32 v49, v50, v49
	v_mov_b32_e32 v50, s28
	v_div_scale_f32 v50, vcc, s32, v50, s32
	v_mul_f32_e32 v51, v50, v49
	v_fma_f32 v52, -v48, v51, v50
	v_fmac_f32_e32 v51, v52, v49
	v_fma_f32 v48, -v48, v51, v50
	v_div_fmas_f32 v48, v48, v49, v51
	v_div_fixup_f32 v48, v48, s28, v47
	v_cmp_gt_f32_e64 vcc, s28, 0
	v_writelane_b32 v40, s28, 13
	s_nop 0
	v_cndmask_b32_e32 v48, 0, v48, vcc
	v_fmaak_f32 v49, v18, v48, 0x4b400000
	v_fmaak_f32 v50, v19, v48, 0x4b400000
	v_fmaak_f32 v51, v20, v48, 0x4b400000
	v_fmaak_f32 v52, v21, v48, 0x4b400000
	v_perm_b32 v49, v50, v49, s33
	v_perm_b32 v51, v52, v51, s34
	v_or_b32_e32 v108, v49, v51
	v_fmaak_f32 v41, v22, v48, 0x4b400000
	v_fmaak_f32 v42, v23, v48, 0x4b400000
	v_fmaak_f32 v43, v24, v48, 0x4b400000
	v_fmaak_f32 v44, v25, v48, 0x4b400000
	v_perm_b32 v41, v42, v41, s33
	v_perm_b32 v43, v44, v43, s34
	v_or_b32_e32 v109, v41, v43
	v_fmaak_f32 v49, v26, v48, 0x4b400000
	v_fmaak_f32 v50, v27, v48, 0x4b400000
	v_fmaak_f32 v51, v28, v48, 0x4b400000
	v_fmaak_f32 v52, v29, v48, 0x4b400000
	v_perm_b32 v49, v50, v49, s33
	v_perm_b32 v51, v52, v51, s34
	v_or_b32_e32 v110, v49, v51
	v_fmaak_f32 v41, v30, v48, 0x4b400000
	v_fmaak_f32 v42, v31, v48, 0x4b400000
	v_fmaak_f32 v43, v32, v48, 0x4b400000
	v_fmaak_f32 v44, v33, v48, 0x4b400000
	v_perm_b32 v41, v42, v41, s33
	v_perm_b32 v43, v44, v43, s34
	v_or_b32_e32 v111, v41, v43
	s_waitcnt vmcnt(0)
	ds_read_b128 v[18:21], v38 offset:0
	ds_read_b128 v[22:25], v38 offset:1024
	ds_read_b128 v[26:29], v38 offset:2048
	ds_read_b128 v[30:33], v38 offset:3072
	s_waitcnt lgkmcnt(0)
	s_mov_b32 m0, s36
	s_nop 0
	global_load_lds_dwordx4 v34, s[16:17] nt
	global_load_lds_dwordx4 v34, s[16:17] offset:1024 nt
	global_load_lds_dwordx4 v34, s[16:17] offset:2048 nt
	global_load_lds_dwordx4 v35, s[16:17] offset:3072 nt
	s_add_u32 s16, s16, 0x7d00
	s_addc_u32 s17, s17, 0
	v_cndmask_b32_e64 v30, 0, v30, s[18:19]
	v_cndmask_b32_e64 v31, 0, v31, s[18:19]
	v_cndmask_b32_e64 v32, 0, v32, s[18:19]
	v_cndmask_b32_e64 v33, 0, v33, s[18:19]
	v_max3_f32 v41, |v18|, |v19|, |v20|
	v_max3_f32 v42, |v21|, |v22|, |v23|
	v_max3_f32 v43, |v24|, |v25|, |v26|
	v_max3_f32 v44, |v27|, |v28|, |v29|
	v_max3_f32 v48, |v30|, |v31|, |v32|
	v_max3_f32 v41, v41, v42, |v33|
	v_max3_f32 v43, v43, v44, v48
	v_max_f32_e32 v41, v41, v43
	v_pk_add_f32 v[2:3], v[2:3], v[18:19]
	v_pk_add_f32 v[4:5], v[4:5], v[20:21]
	v_max_f32_dpp v41, v41, v41 quad_perm:[1,0,3,2] row_mask:0xf bank_mask:0xf
	v_pk_add_f32 v[6:7], v[6:7], v[22:23]
	v_pk_add_f32 v[8:9], v[8:9], v[24:25]
	v_max_f32_dpp v41, v41, v41 quad_perm:[2,3,0,1] row_mask:0xf bank_mask:0xf
	v_pk_add_f32 v[10:11], v[10:11], v[26:27]
	v_pk_add_f32 v[12:13], v[12:13], v[28:29]
	v_max_f32_dpp v41, v41, v41 row_half_mirror row_mask:0xf bank_mask:0xf
	v_pk_add_f32 v[14:15], v[14:15], v[30:31]
	v_pk_add_f32 v[16:17], v[16:17], v[32:33]
	v_max_f32_dpp v41, v41, v41 row_mirror row_mask:0xf bank_mask:0xf
	s_nop 1
	v_max_f32_dpp v41, v41, v41 row_bcast:15 row_mask:0xa bank_mask:0xf
	s_nop 1
	v_max_f32_dpp v41, v41, v41 row_bcast:31 row_mask:0xc bank_mask:0xf
	s_nop 1
	v_readlane_b32 s28, v41, 63
	s_nop 1
	v_div_scale_f32 v48, s[30:31], s28, s28, v47
	v_rcp_f32_e32 v49, v48
	s_nop 0
	v_fma_f32 v50, -v48, v49, 1.0
	v_fmac_f32_e32 v49, v50, v49
	v_mov_b32_e32 v50, s28
	v_div_scale_f32 v50, vcc, s32, v50, s32
	v_mul_f32_e32 v51, v50, v49
	v_fma_f32 v52, -v48, v51, v50
	v_fmac_f32_e32 v51, v52, v49
	v_fma_f32 v48, -v48, v51, v50
	v_div_fmas_f32 v48, v48, v49, v51
	v_div_fixup_f32 v48, v48, s28, v47
	v_cmp_gt_f32_e64 vcc, s28, 0
	v_writelane_b32 v40, s28, 14
	s_nop 0
	v_cndmask_b32_e32 v48, 0, v48, vcc
	v_fmaak_f32 v49, v18, v48, 0x4b400000
	v_fmaak_f32 v50, v19, v48, 0x4b400000
	v_fmaak_f32 v51, v20, v48, 0x4b400000
	v_fmaak_f32 v52, v21, v48, 0x4b400000
	v_perm_b32 v49, v50, v49, s33
	v_perm_b32 v51, v52, v51, s34
	v_or_b32_e32 v112, v49, v51
	v_fmaak_f32 v41, v22, v48, 0x4b400000
	v_fmaak_f32 v42, v23, v48, 0x4b400000
	v_fmaak_f32 v43, v24, v48, 0x4b400000
	v_fmaak_f32 v44, v25, v48, 0x4b400000
	v_perm_b32 v41, v42, v41, s33
	v_perm_b32 v43, v44, v43, s34
	v_or_b32_e32 v113, v41, v43
	v_fmaak_f32 v49, v26, v48, 0x4b400000
	v_fmaak_f32 v50, v27, v48, 0x4b400000
	v_fmaak_f32 v51, v28, v48, 0x4b400000
	v_fmaak_f32 v52, v29, v48, 0x4b400000
	v_perm_b32 v49, v50, v49, s33
	v_perm_b32 v51, v52, v51, s34
	v_or_b32_e32 v114, v49, v51
	v_fmaak_f32 v41, v30, v48, 0x4b400000
	v_fmaak_f32 v42, v31, v48, 0x4b400000
	v_fmaak_f32 v43, v32, v48, 0x4b400000
	v_fmaak_f32 v44, v33, v48, 0x4b400000
	v_perm_b32 v41, v42, v41, s33
	v_perm_b32 v43, v44, v43, s34
	v_or_b32_e32 v115, v41, v43
	s_waitcnt vmcnt(0)
	ds_read_b128 v[18:21], v38 offset:4096
	ds_read_b128 v[22:25], v38 offset:5120
	ds_read_b128 v[26:29], v38 offset:6144
	ds_read_b128 v[30:33], v38 offset:7168
	s_waitcnt lgkmcnt(0)
	s_mov_b32 m0, s35
	s_nop 0
	global_load_lds_dwordx4 v34, s[16:17] nt
	global_load_lds_dwordx4 v34, s[16:17] offset:1024 nt
	global_load_lds_dwordx4 v34, s[16:17] offset:2048 nt
	global_load_lds_dwordx4 v35, s[16:17] offset:3072 nt
	s_add_u32 s16, s16, 0x7d00
	s_addc_u32 s17, s17, 0
	v_cndmask_b32_e64 v30, 0, v30, s[18:19]
	v_cndmask_b32_e64 v31, 0, v31, s[18:19]
	v_cndmask_b32_e64 v32, 0, v32, s[18:19]
	v_cndmask_b32_e64 v33, 0, v33, s[18:19]
	v_max3_f32 v41, |v18|, |v19|, |v20|
	v_max3_f32 v42, |v21|, |v22|, |v23|
	v_max3_f32 v43, |v24|, |v25|, |v26|
	v_max3_f32 v44, |v27|, |v28|, |v29|
	v_max3_f32 v48, |v30|, |v31|, |v32|
	v_max3_f32 v41, v41, v42, |v33|
	v_max3_f32 v43, v43, v44, v48
	v_max_f32_e32 v41, v41, v43
	v_pk_add_f32 v[2:3], v[2:3], v[18:19]
	v_pk_add_f32 v[4:5], v[4:5], v[20:21]
	v_max_f32_dpp v41, v41, v41 quad_perm:[1,0,3,2] row_mask:0xf bank_mask:0xf
	v_pk_add_f32 v[6:7], v[6:7], v[22:23]
	v_pk_add_f32 v[8:9], v[8:9], v[24:25]
	v_max_f32_dpp v41, v41, v41 quad_perm:[2,3,0,1] row_mask:0xf bank_mask:0xf
	v_pk_add_f32 v[10:11], v[10:11], v[26:27]
	v_pk_add_f32 v[12:13], v[12:13], v[28:29]
	v_max_f32_dpp v41, v41, v41 row_half_mirror row_mask:0xf bank_mask:0xf
	v_pk_add_f32 v[14:15], v[14:15], v[30:31]
	v_pk_add_f32 v[16:17], v[16:17], v[32:33]
	v_max_f32_dpp v41, v41, v41 row_mirror row_mask:0xf bank_mask:0xf
	s_nop 1
	v_max_f32_dpp v41, v41, v41 row_bcast:15 row_mask:0xa bank_mask:0xf
	s_nop 1
	v_max_f32_dpp v41, v41, v41 row_bcast:31 row_mask:0xc bank_mask:0xf
	s_nop 1
	v_readlane_b32 s28, v41, 63
	s_nop 1
	v_div_scale_f32 v48, s[30:31], s28, s28, v47
	v_rcp_f32_e32 v49, v48
	s_nop 0
	v_fma_f32 v50, -v48, v49, 1.0
	v_fmac_f32_e32 v49, v50, v49
	v_mov_b32_e32 v50, s28
	v_div_scale_f32 v50, vcc, s32, v50, s32
	v_mul_f32_e32 v51, v50, v49
	v_fma_f32 v52, -v48, v51, v50
	v_fmac_f32_e32 v51, v52, v49
	v_fma_f32 v48, -v48, v51, v50
	v_div_fmas_f32 v48, v48, v49, v51
	v_div_fixup_f32 v48, v48, s28, v47
	v_cmp_gt_f32_e64 vcc, s28, 0
	v_writelane_b32 v40, s28, 15
	s_nop 0
	v_cndmask_b32_e32 v48, 0, v48, vcc
	v_fmaak_f32 v49, v18, v48, 0x4b400000
	v_fmaak_f32 v50, v19, v48, 0x4b400000
	v_fmaak_f32 v51, v20, v48, 0x4b400000
	v_fmaak_f32 v52, v21, v48, 0x4b400000
	v_perm_b32 v49, v50, v49, s33
	v_perm_b32 v51, v52, v51, s34
	v_or_b32_e32 v116, v49, v51
	v_fmaak_f32 v41, v22, v48, 0x4b400000
	v_fmaak_f32 v42, v23, v48, 0x4b400000
	v_fmaak_f32 v43, v24, v48, 0x4b400000
	v_fmaak_f32 v44, v25, v48, 0x4b400000
	v_perm_b32 v41, v42, v41, s33
	v_perm_b32 v43, v44, v43, s34
	v_or_b32_e32 v117, v41, v43
	v_fmaak_f32 v49, v26, v48, 0x4b400000
	v_fmaak_f32 v50, v27, v48, 0x4b400000
	v_fmaak_f32 v51, v28, v48, 0x4b400000
	v_fmaak_f32 v52, v29, v48, 0x4b400000
	v_perm_b32 v49, v50, v49, s33
	v_perm_b32 v51, v52, v51, s34
	v_or_b32_e32 v118, v49, v51
	v_fmaak_f32 v41, v30, v48, 0x4b400000
	v_fmaak_f32 v42, v31, v48, 0x4b400000
	v_fmaak_f32 v43, v32, v48, 0x4b400000
	v_fmaak_f32 v44, v33, v48, 0x4b400000
	v_perm_b32 v41, v42, v41, s33
	v_perm_b32 v43, v44, v43, s34
	v_or_b32_e32 v119, v41, v43
	s_waitcnt vmcnt(0)
	ds_read_b128 v[18:21], v38 offset:0
	ds_read_b128 v[22:25], v38 offset:1024
	ds_read_b128 v[26:29], v38 offset:2048
	ds_read_b128 v[30:33], v38 offset:3072
	s_waitcnt lgkmcnt(0)
	s_mov_b32 m0, s36
	s_nop 0
	global_load_lds_dwordx4 v34, s[16:17] nt
	global_load_lds_dwordx4 v34, s[16:17] offset:1024 nt
	global_load_lds_dwordx4 v34, s[16:17] offset:2048 nt
	global_load_lds_dwordx4 v35, s[16:17] offset:3072 nt
	s_add_u32 s16, s16, 0x7d00
	s_addc_u32 s17, s17, 0
	v_cndmask_b32_e64 v30, 0, v30, s[18:19]
	v_cndmask_b32_e64 v31, 0, v31, s[18:19]
	v_cndmask_b32_e64 v32, 0, v32, s[18:19]
	v_cndmask_b32_e64 v33, 0, v33, s[18:19]
	v_max3_f32 v41, |v18|, |v19|, |v20|
	v_max3_f32 v42, |v21|, |v22|, |v23|
	v_max3_f32 v43, |v24|, |v25|, |v26|
	v_max3_f32 v44, |v27|, |v28|, |v29|
	v_max3_f32 v48, |v30|, |v31|, |v32|
	v_max3_f32 v41, v41, v42, |v33|
	v_max3_f32 v43, v43, v44, v48
	v_max_f32_e32 v41, v41, v43
	v_pk_add_f32 v[2:3], v[2:3], v[18:19]
	v_pk_add_f32 v[4:5], v[4:5], v[20:21]
	v_max_f32_dpp v41, v41, v41 quad_perm:[1,0,3,2] row_mask:0xf bank_mask:0xf
	v_pk_add_f32 v[6:7], v[6:7], v[22:23]
	v_pk_add_f32 v[8:9], v[8:9], v[24:25]
	v_max_f32_dpp v41, v41, v41 quad_perm:[2,3,0,1] row_mask:0xf bank_mask:0xf
	v_pk_add_f32 v[10:11], v[10:11], v[26:27]
	v_pk_add_f32 v[12:13], v[12:13], v[28:29]
	v_max_f32_dpp v41, v41, v41 row_half_mirror row_mask:0xf bank_mask:0xf
	v_pk_add_f32 v[14:15], v[14:15], v[30:31]
	v_pk_add_f32 v[16:17], v[16:17], v[32:33]
	v_max_f32_dpp v41, v41, v41 row_mirror row_mask:0xf bank_mask:0xf
	s_nop 1
	v_max_f32_dpp v41, v41, v41 row_bcast:15 row_mask:0xa bank_mask:0xf
	s_nop 1
	v_max_f32_dpp v41, v41, v41 row_bcast:31 row_mask:0xc bank_mask:0xf
	s_nop 1
	v_readlane_b32 s28, v41, 63
	s_nop 1
	v_div_scale_f32 v48, s[30:31], s28, s28, v47
	v_rcp_f32_e32 v49, v48
	s_nop 0
	v_fma_f32 v50, -v48, v49, 1.0
	v_fmac_f32_e32 v49, v50, v49
	v_mov_b32_e32 v50, s28
	v_div_scale_f32 v50, vcc, s32, v50, s32
	v_mul_f32_e32 v51, v50, v49
	v_fma_f32 v52, -v48, v51, v50
	v_fmac_f32_e32 v51, v52, v49
	v_fma_f32 v48, -v48, v51, v50
	v_div_fmas_f32 v48, v48, v49, v51
	v_div_fixup_f32 v48, v48, s28, v47
	v_cmp_gt_f32_e64 vcc, s28, 0
	v_writelane_b32 v40, s28, 16
	s_nop 0
	v_cndmask_b32_e32 v48, 0, v48, vcc
	v_fmaak_f32 v49, v18, v48, 0x4b400000
	v_fmaak_f32 v50, v19, v48, 0x4b400000
	v_fmaak_f32 v51, v20, v48, 0x4b400000
	v_fmaak_f32 v52, v21, v48, 0x4b400000
	v_perm_b32 v49, v50, v49, s33
	v_perm_b32 v51, v52, v51, s34
	v_or_b32_e32 v120, v49, v51
	v_fmaak_f32 v41, v22, v48, 0x4b400000
	v_fmaak_f32 v42, v23, v48, 0x4b400000
	v_fmaak_f32 v43, v24, v48, 0x4b400000
	v_fmaak_f32 v44, v25, v48, 0x4b400000
	v_perm_b32 v41, v42, v41, s33
	v_perm_b32 v43, v44, v43, s34
	v_or_b32_e32 v121, v41, v43
	v_fmaak_f32 v49, v26, v48, 0x4b400000
	v_fmaak_f32 v50, v27, v48, 0x4b400000
	v_fmaak_f32 v51, v28, v48, 0x4b400000
	v_fmaak_f32 v52, v29, v48, 0x4b400000
	v_perm_b32 v49, v50, v49, s33
	v_perm_b32 v51, v52, v51, s34
	v_or_b32_e32 v122, v49, v51
	v_fmaak_f32 v41, v30, v48, 0x4b400000
	v_fmaak_f32 v42, v31, v48, 0x4b400000
	v_fmaak_f32 v43, v32, v48, 0x4b400000
	v_fmaak_f32 v44, v33, v48, 0x4b400000
	v_perm_b32 v41, v42, v41, s33
	v_perm_b32 v43, v44, v43, s34
	v_or_b32_e32 v123, v41, v43
	s_waitcnt vmcnt(0)
	ds_read_b128 v[18:21], v38 offset:4096
	ds_read_b128 v[22:25], v38 offset:5120
	ds_read_b128 v[26:29], v38 offset:6144
	ds_read_b128 v[30:33], v38 offset:7168
	s_waitcnt lgkmcnt(0)
	s_mov_b32 m0, s35
	s_nop 0
	global_load_lds_dwordx4 v34, s[16:17] nt
	global_load_lds_dwordx4 v34, s[16:17] offset:1024 nt
	global_load_lds_dwordx4 v34, s[16:17] offset:2048 nt
	global_load_lds_dwordx4 v35, s[16:17] offset:3072 nt
	s_add_u32 s16, s16, 0x7d00
	s_addc_u32 s17, s17, 0
	v_cndmask_b32_e64 v30, 0, v30, s[18:19]
	v_cndmask_b32_e64 v31, 0, v31, s[18:19]
	v_cndmask_b32_e64 v32, 0, v32, s[18:19]
	v_cndmask_b32_e64 v33, 0, v33, s[18:19]
	v_max3_f32 v41, |v18|, |v19|, |v20|
	v_max3_f32 v42, |v21|, |v22|, |v23|
	v_max3_f32 v43, |v24|, |v25|, |v26|
	v_max3_f32 v44, |v27|, |v28|, |v29|
	v_max3_f32 v48, |v30|, |v31|, |v32|
	v_max3_f32 v41, v41, v42, |v33|
	v_max3_f32 v43, v43, v44, v48
	v_max_f32_e32 v41, v41, v43
	v_pk_add_f32 v[2:3], v[2:3], v[18:19]
	v_pk_add_f32 v[4:5], v[4:5], v[20:21]
	v_max_f32_dpp v41, v41, v41 quad_perm:[1,0,3,2] row_mask:0xf bank_mask:0xf
	v_pk_add_f32 v[6:7], v[6:7], v[22:23]
	v_pk_add_f32 v[8:9], v[8:9], v[24:25]
	v_max_f32_dpp v41, v41, v41 quad_perm:[2,3,0,1] row_mask:0xf bank_mask:0xf
	v_pk_add_f32 v[10:11], v[10:11], v[26:27]
	v_pk_add_f32 v[12:13], v[12:13], v[28:29]
	v_max_f32_dpp v41, v41, v41 row_half_mirror row_mask:0xf bank_mask:0xf
	v_pk_add_f32 v[14:15], v[14:15], v[30:31]
	v_pk_add_f32 v[16:17], v[16:17], v[32:33]
	v_max_f32_dpp v41, v41, v41 row_mirror row_mask:0xf bank_mask:0xf
	s_nop 1
	v_max_f32_dpp v41, v41, v41 row_bcast:15 row_mask:0xa bank_mask:0xf
	s_nop 1
	v_max_f32_dpp v41, v41, v41 row_bcast:31 row_mask:0xc bank_mask:0xf
	s_nop 1
	v_readlane_b32 s28, v41, 63
	s_nop 1
	v_div_scale_f32 v48, s[30:31], s28, s28, v47
	v_rcp_f32_e32 v49, v48
	s_nop 0
	v_fma_f32 v50, -v48, v49, 1.0
	v_fmac_f32_e32 v49, v50, v49
	v_mov_b32_e32 v50, s28
	v_div_scale_f32 v50, vcc, s32, v50, s32
	v_mul_f32_e32 v51, v50, v49
	v_fma_f32 v52, -v48, v51, v50
	v_fmac_f32_e32 v51, v52, v49
	v_fma_f32 v48, -v48, v51, v50
	v_div_fmas_f32 v48, v48, v49, v51
	v_div_fixup_f32 v48, v48, s28, v47
	v_cmp_gt_f32_e64 vcc, s28, 0
	v_writelane_b32 v40, s28, 17
	s_nop 0
	v_cndmask_b32_e32 v48, 0, v48, vcc
	v_fmaak_f32 v49, v18, v48, 0x4b400000
	v_fmaak_f32 v50, v19, v48, 0x4b400000
	v_fmaak_f32 v51, v20, v48, 0x4b400000
	v_fmaak_f32 v52, v21, v48, 0x4b400000
	v_perm_b32 v49, v50, v49, s33
	v_perm_b32 v51, v52, v51, s34
	v_or_b32_e32 v124, v49, v51
	v_fmaak_f32 v41, v22, v48, 0x4b400000
	v_fmaak_f32 v42, v23, v48, 0x4b400000
	v_fmaak_f32 v43, v24, v48, 0x4b400000
	v_fmaak_f32 v44, v25, v48, 0x4b400000
	v_perm_b32 v41, v42, v41, s33
	v_perm_b32 v43, v44, v43, s34
	v_or_b32_e32 v125, v41, v43
	v_fmaak_f32 v49, v26, v48, 0x4b400000
	v_fmaak_f32 v50, v27, v48, 0x4b400000
	v_fmaak_f32 v51, v28, v48, 0x4b400000
	v_fmaak_f32 v52, v29, v48, 0x4b400000
	v_perm_b32 v49, v50, v49, s33
	v_perm_b32 v51, v52, v51, s34
	v_or_b32_e32 v126, v49, v51
	v_fmaak_f32 v41, v30, v48, 0x4b400000
	v_fmaak_f32 v42, v31, v48, 0x4b400000
	v_fmaak_f32 v43, v32, v48, 0x4b400000
	v_fmaak_f32 v44, v33, v48, 0x4b400000
	v_perm_b32 v41, v42, v41, s33
	v_perm_b32 v43, v44, v43, s34
	v_or_b32_e32 v127, v41, v43
	s_waitcnt vmcnt(0)
	ds_read_b128 v[18:21], v38 offset:0
	ds_read_b128 v[22:25], v38 offset:1024
	ds_read_b128 v[26:29], v38 offset:2048
	ds_read_b128 v[30:33], v38 offset:3072
	s_waitcnt lgkmcnt(0)
	s_mov_b32 m0, s36
	s_nop 0
	global_load_lds_dwordx4 v34, s[16:17] nt
	global_load_lds_dwordx4 v34, s[16:17] offset:1024 nt
	global_load_lds_dwordx4 v34, s[16:17] offset:2048 nt
	global_load_lds_dwordx4 v35, s[16:17] offset:3072 nt
	s_add_u32 s16, s16, 0x7d00
	s_addc_u32 s17, s17, 0
	v_cndmask_b32_e64 v30, 0, v30, s[18:19]
	v_cndmask_b32_e64 v31, 0, v31, s[18:19]
	v_cndmask_b32_e64 v32, 0, v32, s[18:19]
	v_cndmask_b32_e64 v33, 0, v33, s[18:19]
	v_max3_f32 v41, |v18|, |v19|, |v20|
	v_max3_f32 v42, |v21|, |v22|, |v23|
	v_max3_f32 v43, |v24|, |v25|, |v26|
	v_max3_f32 v44, |v27|, |v28|, |v29|
	v_max3_f32 v48, |v30|, |v31|, |v32|
	v_max3_f32 v41, v41, v42, |v33|
	v_max3_f32 v43, v43, v44, v48
	v_max_f32_e32 v41, v41, v43
	v_pk_add_f32 v[2:3], v[2:3], v[18:19]
	v_pk_add_f32 v[4:5], v[4:5], v[20:21]
	v_max_f32_dpp v41, v41, v41 quad_perm:[1,0,3,2] row_mask:0xf bank_mask:0xf
	v_pk_add_f32 v[6:7], v[6:7], v[22:23]
	v_pk_add_f32 v[8:9], v[8:9], v[24:25]
	v_max_f32_dpp v41, v41, v41 quad_perm:[2,3,0,1] row_mask:0xf bank_mask:0xf
	v_pk_add_f32 v[10:11], v[10:11], v[26:27]
	v_pk_add_f32 v[12:13], v[12:13], v[28:29]
	v_max_f32_dpp v41, v41, v41 row_half_mirror row_mask:0xf bank_mask:0xf
	v_pk_add_f32 v[14:15], v[14:15], v[30:31]
	v_pk_add_f32 v[16:17], v[16:17], v[32:33]
	v_max_f32_dpp v41, v41, v41 row_mirror row_mask:0xf bank_mask:0xf
	s_nop 1
	v_max_f32_dpp v41, v41, v41 row_bcast:15 row_mask:0xa bank_mask:0xf
	s_nop 1
	v_max_f32_dpp v41, v41, v41 row_bcast:31 row_mask:0xc bank_mask:0xf
	s_nop 1
	v_readlane_b32 s28, v41, 63
	s_nop 1
	v_div_scale_f32 v48, s[30:31], s28, s28, v47
	v_rcp_f32_e32 v49, v48
	s_nop 0
	v_fma_f32 v50, -v48, v49, 1.0
	v_fmac_f32_e32 v49, v50, v49
	v_mov_b32_e32 v50, s28
	v_div_scale_f32 v50, vcc, s32, v50, s32
	v_mul_f32_e32 v51, v50, v49
	v_fma_f32 v52, -v48, v51, v50
	v_fmac_f32_e32 v51, v52, v49
	v_fma_f32 v48, -v48, v51, v50
	v_div_fmas_f32 v48, v48, v49, v51
	v_div_fixup_f32 v48, v48, s28, v47
	v_cmp_gt_f32_e64 vcc, s28, 0
	v_writelane_b32 v40, s28, 18
	s_nop 0
	v_cndmask_b32_e32 v48, 0, v48, vcc
	v_fmaak_f32 v49, v18, v48, 0x4b400000
	v_fmaak_f32 v50, v19, v48, 0x4b400000
	v_fmaak_f32 v51, v20, v48, 0x4b400000
	v_fmaak_f32 v52, v21, v48, 0x4b400000
	v_perm_b32 v49, v50, v49, s33
	v_perm_b32 v51, v52, v51, s34
	v_or_b32_e32 v36, v49, v51
	v_fmaak_f32 v41, v22, v48, 0x4b400000
	v_fmaak_f32 v42, v23, v48, 0x4b400000
	v_fmaak_f32 v43, v24, v48, 0x4b400000
	v_fmaak_f32 v44, v25, v48, 0x4b400000
	v_perm_b32 v41, v42, v41, s33
	v_perm_b32 v43, v44, v43, s34
	v_or_b32_e32 v37, v41, v43
	v_fmaak_f32 v49, v26, v48, 0x4b400000
	v_fmaak_f32 v50, v27, v48, 0x4b400000
	v_fmaak_f32 v51, v28, v48, 0x4b400000
	v_fmaak_f32 v52, v29, v48, 0x4b400000
	v_perm_b32 v49, v50, v49, s33
	v_perm_b32 v51, v52, v51, s34
	v_or_b32_e32 v45, v49, v51
	v_fmaak_f32 v41, v30, v48, 0x4b400000
	v_fmaak_f32 v42, v31, v48, 0x4b400000
	v_fmaak_f32 v43, v32, v48, 0x4b400000
	v_fmaak_f32 v44, v33, v48, 0x4b400000
	v_perm_b32 v41, v42, v41, s33
	v_perm_b32 v43, v44, v43, s34
	v_or_b32_e32 v46, v41, v43
	s_waitcnt vmcnt(0)
	ds_read_b128 v[18:21], v38 offset:4096
	ds_read_b128 v[22:25], v38 offset:5120
	ds_read_b128 v[26:29], v38 offset:6144
	ds_read_b128 v[30:33], v38 offset:7168
	s_waitcnt lgkmcnt(0)
	s_mov_b32 m0, s35
	s_nop 0
	global_load_lds_dwordx4 v34, s[16:17] nt
	global_load_lds_dwordx4 v34, s[16:17] offset:1024 nt
	global_load_lds_dwordx4 v34, s[16:17] offset:2048 nt
	global_load_lds_dwordx4 v35, s[16:17] offset:3072 nt
	s_add_u32 s16, s16, 0x7d00
	s_addc_u32 s17, s17, 0
	v_cndmask_b32_e64 v30, 0, v30, s[18:19]
	v_cndmask_b32_e64 v31, 0, v31, s[18:19]
	v_cndmask_b32_e64 v32, 0, v32, s[18:19]
	v_cndmask_b32_e64 v33, 0, v33, s[18:19]
	v_max3_f32 v41, |v18|, |v19|, |v20|
	v_max3_f32 v42, |v21|, |v22|, |v23|
	v_max3_f32 v43, |v24|, |v25|, |v26|
	v_max3_f32 v44, |v27|, |v28|, |v29|
	v_max3_f32 v48, |v30|, |v31|, |v32|
	v_max3_f32 v41, v41, v42, |v33|
	v_max3_f32 v43, v43, v44, v48
	v_max_f32_e32 v41, v41, v43
	v_pk_add_f32 v[2:3], v[2:3], v[18:19]
	v_pk_add_f32 v[4:5], v[4:5], v[20:21]
	v_max_f32_dpp v41, v41, v41 quad_perm:[1,0,3,2] row_mask:0xf bank_mask:0xf
	v_pk_add_f32 v[6:7], v[6:7], v[22:23]
	v_pk_add_f32 v[8:9], v[8:9], v[24:25]
	v_max_f32_dpp v41, v41, v41 quad_perm:[2,3,0,1] row_mask:0xf bank_mask:0xf
	v_pk_add_f32 v[10:11], v[10:11], v[26:27]
	v_pk_add_f32 v[12:13], v[12:13], v[28:29]
	v_max_f32_dpp v41, v41, v41 row_half_mirror row_mask:0xf bank_mask:0xf
	v_pk_add_f32 v[14:15], v[14:15], v[30:31]
	v_pk_add_f32 v[16:17], v[16:17], v[32:33]
	v_max_f32_dpp v41, v41, v41 row_mirror row_mask:0xf bank_mask:0xf
	s_nop 1
	v_max_f32_dpp v41, v41, v41 row_bcast:15 row_mask:0xa bank_mask:0xf
	s_nop 1
	v_max_f32_dpp v41, v41, v41 row_bcast:31 row_mask:0xc bank_mask:0xf
	s_nop 1
	v_readlane_b32 s28, v41, 63
	s_nop 1
	v_div_scale_f32 v48, s[30:31], s28, s28, v47
	v_rcp_f32_e32 v49, v48
	s_nop 0
	v_fma_f32 v50, -v48, v49, 1.0
	v_fmac_f32_e32 v49, v50, v49
	v_mov_b32_e32 v50, s28
	v_div_scale_f32 v50, vcc, s32, v50, s32
	v_mul_f32_e32 v51, v50, v49
	v_fma_f32 v52, -v48, v51, v50
	v_fmac_f32_e32 v51, v52, v49
	v_fma_f32 v48, -v48, v51, v50
	v_div_fmas_f32 v48, v48, v49, v51
	v_div_fixup_f32 v48, v48, s28, v47
	v_cmp_gt_f32_e64 vcc, s28, 0
	v_writelane_b32 v40, s28, 19
	s_nop 0
	v_cndmask_b32_e32 v48, 0, v48, vcc
	v_fmaak_f32 v49, v18, v48, 0x4b400000
	v_fmaak_f32 v50, v19, v48, 0x4b400000
	v_fmaak_f32 v51, v20, v48, 0x4b400000
	v_fmaak_f32 v52, v21, v48, 0x4b400000
	v_perm_b32 v49, v50, v49, s33
	v_perm_b32 v51, v52, v51, s34
	v_or_b32_e32 v53, v49, v51
	v_fmaak_f32 v41, v22, v48, 0x4b400000
	v_fmaak_f32 v42, v23, v48, 0x4b400000
	v_fmaak_f32 v43, v24, v48, 0x4b400000
	v_fmaak_f32 v44, v25, v48, 0x4b400000
	v_perm_b32 v41, v42, v41, s33
	v_perm_b32 v43, v44, v43, s34
	v_or_b32_e32 v54, v41, v43
	v_fmaak_f32 v49, v26, v48, 0x4b400000
	v_fmaak_f32 v50, v27, v48, 0x4b400000
	v_fmaak_f32 v51, v28, v48, 0x4b400000
	v_fmaak_f32 v52, v29, v48, 0x4b400000
	v_perm_b32 v49, v50, v49, s33
	v_perm_b32 v51, v52, v51, s34
	v_or_b32_e32 v55, v49, v51
	v_fmaak_f32 v41, v30, v48, 0x4b400000
	v_fmaak_f32 v42, v31, v48, 0x4b400000
	v_fmaak_f32 v43, v32, v48, 0x4b400000
	v_fmaak_f32 v44, v33, v48, 0x4b400000
	v_perm_b32 v41, v42, v41, s33
	v_perm_b32 v43, v44, v43, s34
	v_or_b32_e32 v1, v41, v43
	s_waitcnt vmcnt(0)
	ds_read_b128 v[18:21], v38 offset:0
	ds_read_b128 v[22:25], v38 offset:1024
	ds_read_b128 v[26:29], v38 offset:2048
	ds_read_b128 v[30:33], v38 offset:3072
	s_waitcnt lgkmcnt(0)
	s_mov_b32 m0, s36
	s_nop 0
	global_load_lds_dwordx4 v34, s[16:17] nt
	global_load_lds_dwordx4 v34, s[16:17] offset:1024 nt
	global_load_lds_dwordx4 v34, s[16:17] offset:2048 nt
	global_load_lds_dwordx4 v35, s[16:17] offset:3072 nt
	s_add_u32 s16, s16, 0x7d00
	s_addc_u32 s17, s17, 0
	v_cndmask_b32_e64 v30, 0, v30, s[18:19]
	v_cndmask_b32_e64 v31, 0, v31, s[18:19]
	v_cndmask_b32_e64 v32, 0, v32, s[18:19]
	v_cndmask_b32_e64 v33, 0, v33, s[18:19]
	v_max3_f32 v41, |v18|, |v19|, |v20|
	v_max3_f32 v42, |v21|, |v22|, |v23|
	v_max3_f32 v43, |v24|, |v25|, |v26|
	v_max3_f32 v44, |v27|, |v28|, |v29|
	v_max3_f32 v48, |v30|, |v31|, |v32|
	v_max3_f32 v41, v41, v42, |v33|
	v_max3_f32 v43, v43, v44, v48
	v_max_f32_e32 v41, v41, v43
	v_pk_add_f32 v[2:3], v[2:3], v[18:19]
	v_pk_add_f32 v[4:5], v[4:5], v[20:21]
	v_max_f32_dpp v41, v41, v41 quad_perm:[1,0,3,2] row_mask:0xf bank_mask:0xf
	v_pk_add_f32 v[6:7], v[6:7], v[22:23]
	v_pk_add_f32 v[8:9], v[8:9], v[24:25]
	v_max_f32_dpp v41, v41, v41 quad_perm:[2,3,0,1] row_mask:0xf bank_mask:0xf
	v_pk_add_f32 v[10:11], v[10:11], v[26:27]
	v_pk_add_f32 v[12:13], v[12:13], v[28:29]
	v_max_f32_dpp v41, v41, v41 row_half_mirror row_mask:0xf bank_mask:0xf
	v_pk_add_f32 v[14:15], v[14:15], v[30:31]
	v_pk_add_f32 v[16:17], v[16:17], v[32:33]
	v_max_f32_dpp v41, v41, v41 row_mirror row_mask:0xf bank_mask:0xf
	s_nop 1
	v_max_f32_dpp v41, v41, v41 row_bcast:15 row_mask:0xa bank_mask:0xf
	s_nop 1
	v_max_f32_dpp v41, v41, v41 row_bcast:31 row_mask:0xc bank_mask:0xf
	s_nop 1
	v_readlane_b32 s28, v41, 63
	s_nop 1
	v_div_scale_f32 v48, s[30:31], s28, s28, v47
	v_rcp_f32_e32 v49, v48
	s_nop 0
	v_fma_f32 v50, -v48, v49, 1.0
	v_fmac_f32_e32 v49, v50, v49
	v_mov_b32_e32 v50, s28
	v_div_scale_f32 v50, vcc, s32, v50, s32
	v_mul_f32_e32 v51, v50, v49
	v_fma_f32 v52, -v48, v51, v50
	v_fmac_f32_e32 v51, v52, v49
	v_fma_f32 v48, -v48, v51, v50
	v_div_fmas_f32 v48, v48, v49, v51
	v_div_fixup_f32 v48, v48, s28, v47
	v_cmp_gt_f32_e64 vcc, s28, 0
	v_writelane_b32 v40, s28, 20
	s_nop 0
	v_cndmask_b32_e32 v48, 0, v48, vcc
	v_fmaak_f32 v49, v18, v48, 0x4b400000
	v_fmaak_f32 v50, v19, v48, 0x4b400000
	v_fmaak_f32 v51, v20, v48, 0x4b400000
	v_fmaak_f32 v52, v21, v48, 0x4b400000
	v_perm_b32 v49, v50, v49, s33
	v_perm_b32 v51, v52, v51, s34
	v_or_b32_e32 v49, v49, v51
	s_add_u32 s20, s20, 0x5000
	s_addc_u32 s21, s21, 0
	s_add_u32 s22, s22, 0x5000
	s_addc_u32 s23, s23, 0
	s_add_u32 s24, s24, 0x5000
	s_addc_u32 s25, s25, 0
	s_add_u32 s26, s26, 0x5000
	s_addc_u32 s27, s27, 0
	global_store_dword v39, v49, s[20:21]
	v_fmaak_f32 v41, v22, v48, 0x4b400000
	v_fmaak_f32 v42, v23, v48, 0x4b400000
	v_fmaak_f32 v43, v24, v48, 0x4b400000
	v_fmaak_f32 v44, v25, v48, 0x4b400000
	v_perm_b32 v41, v42, v41, s33
	v_perm_b32 v43, v44, v43, s34
	v_or_b32_e32 v41, v41, v43
	global_store_dword v39, v41, s[22:23]
	v_fmaak_f32 v49, v26, v48, 0x4b400000
	v_fmaak_f32 v50, v27, v48, 0x4b400000
	v_fmaak_f32 v51, v28, v48, 0x4b400000
	v_fmaak_f32 v52, v29, v48, 0x4b400000
	v_perm_b32 v49, v50, v49, s33
	v_perm_b32 v51, v52, v51, s34
	v_or_b32_e32 v49, v49, v51
	global_store_dword v39, v49, s[24:25]
	v_fmaak_f32 v41, v30, v48, 0x4b400000
	v_fmaak_f32 v42, v31, v48, 0x4b400000
	v_fmaak_f32 v43, v32, v48, 0x4b400000
	v_fmaak_f32 v44, v33, v48, 0x4b400000
	v_perm_b32 v41, v42, v41, s33
	v_perm_b32 v43, v44, v43, s34
	v_or_b32_e32 v41, v41, v43
	global_store_dword v39, v41, s[26:27]
	s_waitcnt vmcnt(4)
	ds_read_b128 v[18:21], v38 offset:4096
	ds_read_b128 v[22:25], v38 offset:5120
	ds_read_b128 v[26:29], v38 offset:6144
	ds_read_b128 v[30:33], v38 offset:7168
	s_waitcnt lgkmcnt(0)
	s_mov_b32 m0, s35
	s_nop 0
	global_load_lds_dwordx4 v34, s[16:17] nt
	global_load_lds_dwordx4 v34, s[16:17] offset:1024 nt
	global_load_lds_dwordx4 v34, s[16:17] offset:2048 nt
	global_load_lds_dwordx4 v35, s[16:17] offset:3072 nt
	s_add_u32 s16, s16, 0x7d00
	s_addc_u32 s17, s17, 0
	v_cndmask_b32_e64 v30, 0, v30, s[18:19]
	v_cndmask_b32_e64 v31, 0, v31, s[18:19]
	v_cndmask_b32_e64 v32, 0, v32, s[18:19]
	v_cndmask_b32_e64 v33, 0, v33, s[18:19]
	v_max3_f32 v41, |v18|, |v19|, |v20|
	v_max3_f32 v42, |v21|, |v22|, |v23|
	v_max3_f32 v43, |v24|, |v25|, |v26|
	v_max3_f32 v44, |v27|, |v28|, |v29|
	v_max3_f32 v48, |v30|, |v31|, |v32|
	v_max3_f32 v41, v41, v42, |v33|
	v_max3_f32 v43, v43, v44, v48
	v_max_f32_e32 v41, v41, v43
	v_pk_add_f32 v[2:3], v[2:3], v[18:19]
	v_pk_add_f32 v[4:5], v[4:5], v[20:21]
	v_max_f32_dpp v41, v41, v41 quad_perm:[1,0,3,2] row_mask:0xf bank_mask:0xf
	v_pk_add_f32 v[6:7], v[6:7], v[22:23]
	v_pk_add_f32 v[8:9], v[8:9], v[24:25]
	v_max_f32_dpp v41, v41, v41 quad_perm:[2,3,0,1] row_mask:0xf bank_mask:0xf
	v_pk_add_f32 v[10:11], v[10:11], v[26:27]
	v_pk_add_f32 v[12:13], v[12:13], v[28:29]
	v_max_f32_dpp v41, v41, v41 row_half_mirror row_mask:0xf bank_mask:0xf
	v_pk_add_f32 v[14:15], v[14:15], v[30:31]
	v_pk_add_f32 v[16:17], v[16:17], v[32:33]
	v_max_f32_dpp v41, v41, v41 row_mirror row_mask:0xf bank_mask:0xf
	s_nop 1
	v_max_f32_dpp v41, v41, v41 row_bcast:15 row_mask:0xa bank_mask:0xf
	s_nop 1
	v_max_f32_dpp v41, v41, v41 row_bcast:31 row_mask:0xc bank_mask:0xf
	s_nop 1
	v_readlane_b32 s28, v41, 63
	s_nop 1
	v_div_scale_f32 v48, s[30:31], s28, s28, v47
	v_rcp_f32_e32 v49, v48
	s_nop 0
	v_fma_f32 v50, -v48, v49, 1.0
	v_fmac_f32_e32 v49, v50, v49
	v_mov_b32_e32 v50, s28
	v_div_scale_f32 v50, vcc, s32, v50, s32
	v_mul_f32_e32 v51, v50, v49
	v_fma_f32 v52, -v48, v51, v50
	v_fmac_f32_e32 v51, v52, v49
	v_fma_f32 v48, -v48, v51, v50
	v_div_fmas_f32 v48, v48, v49, v51
	v_div_fixup_f32 v48, v48, s28, v47
	v_cmp_gt_f32_e64 vcc, s28, 0
	v_writelane_b32 v40, s28, 21
	s_nop 0
	v_cndmask_b32_e32 v48, 0, v48, vcc
	v_fmaak_f32 v49, v18, v48, 0x4b400000
	v_fmaak_f32 v50, v19, v48, 0x4b400000
	v_fmaak_f32 v51, v20, v48, 0x4b400000
	v_fmaak_f32 v52, v21, v48, 0x4b400000
	v_perm_b32 v49, v50, v49, s33
	v_perm_b32 v51, v52, v51, s34
	v_or_b32_e32 v49, v49, v51
	s_add_u32 s20, s20, 0x400
	s_addc_u32 s21, s21, 0
	s_add_u32 s22, s22, 0x400
	s_addc_u32 s23, s23, 0
	s_add_u32 s24, s24, 0x400
	s_addc_u32 s25, s25, 0
	s_add_u32 s26, s26, 0x400
	s_addc_u32 s27, s27, 0
	global_store_dword v39, v49, s[20:21]
	v_fmaak_f32 v41, v22, v48, 0x4b400000
	v_fmaak_f32 v42, v23, v48, 0x4b400000
	v_fmaak_f32 v43, v24, v48, 0x4b400000
	v_fmaak_f32 v44, v25, v48, 0x4b400000
	v_perm_b32 v41, v42, v41, s33
	v_perm_b32 v43, v44, v43, s34
	v_or_b32_e32 v41, v41, v43
	global_store_dword v39, v41, s[22:23]
	v_fmaak_f32 v49, v26, v48, 0x4b400000
	v_fmaak_f32 v50, v27, v48, 0x4b400000
	v_fmaak_f32 v51, v28, v48, 0x4b400000
	v_fmaak_f32 v52, v29, v48, 0x4b400000
	v_perm_b32 v49, v50, v49, s33
	v_perm_b32 v51, v52, v51, s34
	v_or_b32_e32 v49, v49, v51
	global_store_dword v39, v49, s[24:25]
	v_fmaak_f32 v41, v30, v48, 0x4b400000
	v_fmaak_f32 v42, v31, v48, 0x4b400000
	v_fmaak_f32 v43, v32, v48, 0x4b400000
	v_fmaak_f32 v44, v33, v48, 0x4b400000
	v_perm_b32 v41, v42, v41, s33
	v_perm_b32 v43, v44, v43, s34
	v_or_b32_e32 v41, v41, v43
	global_store_dword v39, v41, s[26:27]
	s_waitcnt vmcnt(4)
	ds_read_b128 v[18:21], v38 offset:0
	ds_read_b128 v[22:25], v38 offset:1024
	ds_read_b128 v[26:29], v38 offset:2048
	ds_read_b128 v[30:33], v38 offset:3072
	s_waitcnt lgkmcnt(0)
	s_mov_b32 m0, s36
	s_nop 0
	global_load_lds_dwordx4 v34, s[16:17] nt
	global_load_lds_dwordx4 v34, s[16:17] offset:1024 nt
	global_load_lds_dwordx4 v34, s[16:17] offset:2048 nt
	global_load_lds_dwordx4 v35, s[16:17] offset:3072 nt
	s_add_u32 s16, s16, 0x7d00
	s_addc_u32 s17, s17, 0
	v_cndmask_b32_e64 v30, 0, v30, s[18:19]
	v_cndmask_b32_e64 v31, 0, v31, s[18:19]
	v_cndmask_b32_e64 v32, 0, v32, s[18:19]
	v_cndmask_b32_e64 v33, 0, v33, s[18:19]
	v_max3_f32 v41, |v18|, |v19|, |v20|
	v_max3_f32 v42, |v21|, |v22|, |v23|
	v_max3_f32 v43, |v24|, |v25|, |v26|
	v_max3_f32 v44, |v27|, |v28|, |v29|
	v_max3_f32 v48, |v30|, |v31|, |v32|
	v_max3_f32 v41, v41, v42, |v33|
	v_max3_f32 v43, v43, v44, v48
	v_max_f32_e32 v41, v41, v43
	v_pk_add_f32 v[2:3], v[2:3], v[18:19]
	v_pk_add_f32 v[4:5], v[4:5], v[20:21]
	v_max_f32_dpp v41, v41, v41 quad_perm:[1,0,3,2] row_mask:0xf bank_mask:0xf
	v_pk_add_f32 v[6:7], v[6:7], v[22:23]
	v_pk_add_f32 v[8:9], v[8:9], v[24:25]
	v_max_f32_dpp v41, v41, v41 quad_perm:[2,3,0,1] row_mask:0xf bank_mask:0xf
	v_pk_add_f32 v[10:11], v[10:11], v[26:27]
	v_pk_add_f32 v[12:13], v[12:13], v[28:29]
	v_max_f32_dpp v41, v41, v41 row_half_mirror row_mask:0xf bank_mask:0xf
	v_pk_add_f32 v[14:15], v[14:15], v[30:31]
	v_pk_add_f32 v[16:17], v[16:17], v[32:33]
	v_max_f32_dpp v41, v41, v41 row_mirror row_mask:0xf bank_mask:0xf
	s_nop 1
	v_max_f32_dpp v41, v41, v41 row_bcast:15 row_mask:0xa bank_mask:0xf
	s_nop 1
	v_max_f32_dpp v41, v41, v41 row_bcast:31 row_mask:0xc bank_mask:0xf
	s_nop 1
	v_readlane_b32 s28, v41, 63
	s_nop 1
	v_div_scale_f32 v48, s[30:31], s28, s28, v47
	v_rcp_f32_e32 v49, v48
	s_nop 0
	v_fma_f32 v50, -v48, v49, 1.0
	v_fmac_f32_e32 v49, v50, v49
	v_mov_b32_e32 v50, s28
	v_div_scale_f32 v50, vcc, s32, v50, s32
	v_mul_f32_e32 v51, v50, v49
	v_fma_f32 v52, -v48, v51, v50
	v_fmac_f32_e32 v51, v52, v49
	v_fma_f32 v48, -v48, v51, v50
	v_div_fmas_f32 v48, v48, v49, v51
	v_div_fixup_f32 v48, v48, s28, v47
	v_cmp_gt_f32_e64 vcc, s28, 0
	v_writelane_b32 v40, s28, 22
	s_nop 0
	v_cndmask_b32_e32 v48, 0, v48, vcc
	v_fmaak_f32 v49, v18, v48, 0x4b400000
	v_fmaak_f32 v50, v19, v48, 0x4b400000
	v_fmaak_f32 v51, v20, v48, 0x4b400000
	v_fmaak_f32 v52, v21, v48, 0x4b400000
	v_perm_b32 v49, v50, v49, s33
	v_perm_b32 v51, v52, v51, s34
	v_or_b32_e32 v49, v49, v51
	s_add_u32 s20, s20, 0x400
	s_addc_u32 s21, s21, 0
	s_add_u32 s22, s22, 0x400
	s_addc_u32 s23, s23, 0
	s_add_u32 s24, s24, 0x400
	s_addc_u32 s25, s25, 0
	s_add_u32 s26, s26, 0x400
	s_addc_u32 s27, s27, 0
	global_store_dword v39, v49, s[20:21]
	v_fmaak_f32 v41, v22, v48, 0x4b400000
	v_fmaak_f32 v42, v23, v48, 0x4b400000
	v_fmaak_f32 v43, v24, v48, 0x4b400000
	v_fmaak_f32 v44, v25, v48, 0x4b400000
	v_perm_b32 v41, v42, v41, s33
	v_perm_b32 v43, v44, v43, s34
	v_or_b32_e32 v41, v41, v43
	global_store_dword v39, v41, s[22:23]
	v_fmaak_f32 v49, v26, v48, 0x4b400000
	v_fmaak_f32 v50, v27, v48, 0x4b400000
	v_fmaak_f32 v51, v28, v48, 0x4b400000
	v_fmaak_f32 v52, v29, v48, 0x4b400000
	v_perm_b32 v49, v50, v49, s33
	v_perm_b32 v51, v52, v51, s34
	v_or_b32_e32 v49, v49, v51
	global_store_dword v39, v49, s[24:25]
	v_fmaak_f32 v41, v30, v48, 0x4b400000
	v_fmaak_f32 v42, v31, v48, 0x4b400000
	v_fmaak_f32 v43, v32, v48, 0x4b400000
	v_fmaak_f32 v44, v33, v48, 0x4b400000
	v_perm_b32 v41, v42, v41, s33
	v_perm_b32 v43, v44, v43, s34
	v_or_b32_e32 v41, v41, v43
	global_store_dword v39, v41, s[26:27]
	s_waitcnt vmcnt(4)
	ds_read_b128 v[18:21], v38 offset:4096
	ds_read_b128 v[22:25], v38 offset:5120
	ds_read_b128 v[26:29], v38 offset:6144
	ds_read_b128 v[30:33], v38 offset:7168
	s_waitcnt lgkmcnt(0)
	s_cmp_eq_u32 s29, 1
	s_cbranch_scc0 .Lk1_nodma24
	s_mov_b32 m0, s35
	s_nop 0
	global_load_lds_dwordx4 v34, s[16:17] nt
	global_load_lds_dwordx4 v34, s[16:17] offset:1024 nt
	global_load_lds_dwordx4 v34, s[16:17] offset:2048 nt
	global_load_lds_dwordx4 v35, s[16:17] offset:3072 nt
	s_add_u32 s16, s16, 0x7d00
	s_addc_u32 s17, s17, 0
.Lk1_nodma24:
	v_cndmask_b32_e64 v30, 0, v30, s[18:19]
	v_cndmask_b32_e64 v31, 0, v31, s[18:19]
	v_cndmask_b32_e64 v32, 0, v32, s[18:19]
	v_cndmask_b32_e64 v33, 0, v33, s[18:19]
	v_max3_f32 v41, |v18|, |v19|, |v20|
	v_max3_f32 v42, |v21|, |v22|, |v23|
	v_max3_f32 v43, |v24|, |v25|, |v26|
	v_max3_f32 v44, |v27|, |v28|, |v29|
	v_max3_f32 v48, |v30|, |v31|, |v32|
	v_max3_f32 v41, v41, v42, |v33|
	v_max3_f32 v43, v43, v44, v48
	v_max_f32_e32 v41, v41, v43
	v_pk_add_f32 v[2:3], v[2:3], v[18:19]
	v_pk_add_f32 v[4:5], v[4:5], v[20:21]
	v_max_f32_dpp v41, v41, v41 quad_perm:[1,0,3,2] row_mask:0xf bank_mask:0xf
	v_pk_add_f32 v[6:7], v[6:7], v[22:23]
	v_pk_add_f32 v[8:9], v[8:9], v[24:25]
	v_max_f32_dpp v41, v41, v41 quad_perm:[2,3,0,1] row_mask:0xf bank_mask:0xf
	v_pk_add_f32 v[10:11], v[10:11], v[26:27]
	v_pk_add_f32 v[12:13], v[12:13], v[28:29]
	v_max_f32_dpp v41, v41, v41 row_half_mirror row_mask:0xf bank_mask:0xf
	v_pk_add_f32 v[14:15], v[14:15], v[30:31]
	v_pk_add_f32 v[16:17], v[16:17], v[32:33]
	v_max_f32_dpp v41, v41, v41 row_mirror row_mask:0xf bank_mask:0xf
	s_nop 1
	v_max_f32_dpp v41, v41, v41 row_bcast:15 row_mask:0xa bank_mask:0xf
	s_nop 1
	v_max_f32_dpp v41, v41, v41 row_bcast:31 row_mask:0xc bank_mask:0xf
	s_nop 1
	v_readlane_b32 s28, v41, 63
	s_nop 1
	v_div_scale_f32 v48, s[30:31], s28, s28, v47
	v_rcp_f32_e32 v49, v48
	s_nop 0
	v_fma_f32 v50, -v48, v49, 1.0
	v_fmac_f32_e32 v49, v50, v49
	v_mov_b32_e32 v50, s28
	v_div_scale_f32 v50, vcc, s32, v50, s32
	v_mul_f32_e32 v51, v50, v49
	v_fma_f32 v52, -v48, v51, v50
	v_fmac_f32_e32 v51, v52, v49
	v_fma_f32 v48, -v48, v51, v50
	v_div_fmas_f32 v48, v48, v49, v51
	v_div_fixup_f32 v48, v48, s28, v47
	v_cmp_gt_f32_e64 vcc, s28, 0
	v_writelane_b32 v40, s28, 23
	s_nop 0
	v_cndmask_b32_e32 v48, 0, v48, vcc
	v_fmaak_f32 v49, v18, v48, 0x4b400000
	v_fmaak_f32 v50, v19, v48, 0x4b400000
	v_fmaak_f32 v51, v20, v48, 0x4b400000
	v_fmaak_f32 v52, v21, v48, 0x4b400000
	v_perm_b32 v49, v50, v49, s33
	v_perm_b32 v51, v52, v51, s34
	v_or_b32_e32 v49, v49, v51
	s_add_u32 s20, s20, 0x400
	s_addc_u32 s21, s21, 0
	s_add_u32 s22, s22, 0x400
	s_addc_u32 s23, s23, 0
	s_add_u32 s24, s24, 0x400
	s_addc_u32 s25, s25, 0
	s_add_u32 s26, s26, 0x400
	s_addc_u32 s27, s27, 0
	global_store_dword v39, v49, s[20:21]
	v_fmaak_f32 v41, v22, v48, 0x4b400000
	v_fmaak_f32 v42, v23, v48, 0x4b400000
	v_fmaak_f32 v43, v24, v48, 0x4b400000
	v_fmaak_f32 v44, v25, v48, 0x4b400000
	v_perm_b32 v41, v42, v41, s33
	v_perm_b32 v43, v44, v43, s34
	v_or_b32_e32 v41, v41, v43
	global_store_dword v39, v41, s[22:23]
	v_fmaak_f32 v49, v26, v48, 0x4b400000
	v_fmaak_f32 v50, v27, v48, 0x4b400000
	v_fmaak_f32 v51, v28, v48, 0x4b400000
	v_fmaak_f32 v52, v29, v48, 0x4b400000
	v_perm_b32 v49, v50, v49, s33
	v_perm_b32 v51, v52, v51, s34
	v_or_b32_e32 v49, v49, v51
	global_store_dword v39, v49, s[24:25]
	v_fmaak_f32 v41, v30, v48, 0x4b400000
	v_fmaak_f32 v42, v31, v48, 0x4b400000
	v_fmaak_f32 v43, v32, v48, 0x4b400000
	v_fmaak_f32 v44, v33, v48, 0x4b400000
	v_perm_b32 v41, v42, v41, s33
	v_perm_b32 v43, v44, v43, s34
	v_or_b32_e32 v41, v41, v43
	global_store_dword v39, v41, s[26:27]
	s_cmp_eq_u32 s29, 1
	s_cbranch_scc0 .Lk1_flush
	s_waitcnt vmcnt(4)
	ds_read_b128 v[18:21], v38 offset:0
	ds_read_b128 v[22:25], v38 offset:1024
	ds_read_b128 v[26:29], v38 offset:2048
	ds_read_b128 v[30:33], v38 offset:3072
	s_waitcnt lgkmcnt(0)
	v_cndmask_b32_e64 v30, 0, v30, s[18:19]
	v_cndmask_b32_e64 v31, 0, v31, s[18:19]
	v_cndmask_b32_e64 v32, 0, v32, s[18:19]
	v_cndmask_b32_e64 v33, 0, v33, s[18:19]
	v_max3_f32 v41, |v18|, |v19|, |v20|
	v_max3_f32 v42, |v21|, |v22|, |v23|
	v_max3_f32 v43, |v24|, |v25|, |v26|
	v_max3_f32 v44, |v27|, |v28|, |v29|
	v_max3_f32 v48, |v30|, |v31|, |v32|
	v_max3_f32 v41, v41, v42, |v33|
	v_max3_f32 v43, v43, v44, v48
	v_max_f32_e32 v41, v41, v43
	v_pk_add_f32 v[2:3], v[2:3], v[18:19]
	v_pk_add_f32 v[4:5], v[4:5], v[20:21]
	v_max_f32_dpp v41, v41, v41 quad_perm:[1,0,3,2] row_mask:0xf bank_mask:0xf
	v_pk_add_f32 v[6:7], v[6:7], v[22:23]
	v_pk_add_f32 v[8:9], v[8:9], v[24:25]
	v_max_f32_dpp v41, v41, v41 quad_perm:[2,3,0,1] row_mask:0xf bank_mask:0xf
	v_pk_add_f32 v[10:11], v[10:11], v[26:27]
	v_pk_add_f32 v[12:13], v[12:13], v[28:29]
	v_max_f32_dpp v41, v41, v41 row_half_mirror row_mask:0xf bank_mask:0xf
	v_pk_add_f32 v[14:15], v[14:15], v[30:31]
	v_pk_add_f32 v[16:17], v[16:17], v[32:33]
	v_max_f32_dpp v41, v41, v41 row_mirror row_mask:0xf bank_mask:0xf
	s_nop 1
	v_max_f32_dpp v41, v41, v41 row_bcast:15 row_mask:0xa bank_mask:0xf
	s_nop 1
	v_max_f32_dpp v41, v41, v41 row_bcast:31 row_mask:0xc bank_mask:0xf
	s_nop 1
	v_readlane_b32 s28, v41, 63
	s_nop 1
	v_div_scale_f32 v48, s[30:31], s28, s28, v47
	v_rcp_f32_e32 v49, v48
	s_nop 0
	v_fma_f32 v50, -v48, v49, 1.0
	v_fmac_f32_e32 v49, v50, v49
	v_mov_b32_e32 v50, s28
	v_div_scale_f32 v50, vcc, s32, v50, s32
	v_mul_f32_e32 v51, v50, v49
	v_fma_f32 v52, -v48, v51, v50
	v_fmac_f32_e32 v51, v52, v49
	v_fma_f32 v48, -v48, v51, v50
	v_div_fmas_f32 v48, v48, v49, v51
	v_div_fixup_f32 v48, v48, s28, v47
	v_cmp_gt_f32_e64 vcc, s28, 0
	v_writelane_b32 v40, s28, 24
	s_nop 0
	v_cndmask_b32_e32 v48, 0, v48, vcc
	v_fmaak_f32 v49, v18, v48, 0x4b400000
	v_fmaak_f32 v50, v19, v48, 0x4b400000
	v_fmaak_f32 v51, v20, v48, 0x4b400000
	v_fmaak_f32 v52, v21, v48, 0x4b400000
	v_perm_b32 v49, v50, v49, s33
	v_perm_b32 v51, v52, v51, s34
	v_or_b32_e32 v49, v49, v51
	s_add_u32 s20, s20, 0x400
	s_addc_u32 s21, s21, 0
	s_add_u32 s22, s22, 0x400
	s_addc_u32 s23, s23, 0
	s_add_u32 s24, s24, 0x400
	s_addc_u32 s25, s25, 0
	s_add_u32 s26, s26, 0x400
	s_addc_u32 s27, s27, 0
	global_store_dword v39, v49, s[20:21]
	v_fmaak_f32 v41, v22, v48, 0x4b400000
	v_fmaak_f32 v42, v23, v48, 0x4b400000
	v_fmaak_f32 v43, v24, v48, 0x4b400000
	v_fmaak_f32 v44, v25, v48, 0x4b400000
	v_perm_b32 v41, v42, v41, s33
	v_perm_b32 v43, v44, v43, s34
	v_or_b32_e32 v41, v41, v43
	global_store_dword v39, v41, s[22:23]
	v_fmaak_f32 v49, v26, v48, 0x4b400000
	v_fmaak_f32 v50, v27, v48, 0x4b400000
	v_fmaak_f32 v51, v28, v48, 0x4b400000
	v_fmaak_f32 v52, v29, v48, 0x4b400000
	v_perm_b32 v49, v50, v49, s33
	v_perm_b32 v51, v52, v51, s34
	v_or_b32_e32 v49, v49, v51
	global_store_dword v39, v49, s[24:25]
	v_fmaak_f32 v41, v30, v48, 0x4b400000
	v_fmaak_f32 v42, v31, v48, 0x4b400000
	v_fmaak_f32 v43, v32, v48, 0x4b400000
	v_fmaak_f32 v44, v33, v48, 0x4b400000
	v_perm_b32 v41, v42, v41, s33
	v_perm_b32 v43, v44, v43, s34
	v_or_b32_e32 v41, v41, v43
	global_store_dword v39, v41, s[26:27]
.Lk1_flush:
	s_add_u32 s20, s40, 0x0
	s_addc_u32 s21, s41, 0
	s_add_u32 s22, s20, 0x186a000
	s_addc_u32 s23, s21, 0
	s_add_u32 s24, s22, 0x186a000
	s_addc_u32 s25, s23, 0
	s_add_u32 s26, s24, 0x186a000
	s_addc_u32 s27, s25, 0
	global_store_dword v39, v56, s[20:21] sc1
	global_store_dword v39, v57, s[22:23] sc1
	global_store_dword v39, v58, s[24:25] sc1
	global_store_dword v39, v59, s[26:27] sc1
	global_store_dword v39, v60, s[20:21] offset:1024 sc1
	global_store_dword v39, v61, s[22:23] offset:1024 sc1
	global_store_dword v39, v62, s[24:25] offset:1024 sc1
	global_store_dword v39, v63, s[26:27] offset:1024 sc1
	global_store_dword v39, v64, s[20:21] offset:2048 sc1
	global_store_dword v39, v65, s[22:23] offset:2048 sc1
	global_store_dword v39, v66, s[24:25] offset:2048 sc1
	global_store_dword v39, v67, s[26:27] offset:2048 sc1
	global_store_dword v39, v68, s[20:21] offset:3072 sc1
	global_store_dword v39, v69, s[22:23] offset:3072 sc1
	global_store_dword v39, v70, s[24:25] offset:3072 sc1
	global_store_dword v39, v71, s[26:27] offset:3072 sc1
	s_add_u32 s20, s20, 0x1000
	s_addc_u32 s21, s21, 0
	s_add_u32 s22, s22, 0x1000
	s_addc_u32 s23, s23, 0
	s_add_u32 s24, s24, 0x1000
	s_addc_u32 s25, s25, 0
	s_add_u32 s26, s26, 0x1000
	s_addc_u32 s27, s27, 0
	global_store_dword v39, v72, s[20:21] sc1
	global_store_dword v39, v73, s[22:23] sc1
	global_store_dword v39, v74, s[24:25] sc1
	global_store_dword v39, v75, s[26:27] sc1
	global_store_dword v39, v76, s[20:21] offset:1024 sc1
	global_store_dword v39, v77, s[22:23] offset:1024 sc1
	global_store_dword v39, v78, s[24:25] offset:1024 sc1
	global_store_dword v39, v79, s[26:27] offset:1024 sc1
	global_store_dword v39, v80, s[20:21] offset:2048 sc1
	global_store_dword v39, v81, s[22:23] offset:2048 sc1
	global_store_dword v39, v82, s[24:25] offset:2048 sc1
	global_store_dword v39, v83, s[26:27] offset:2048 sc1
	global_store_dword v39, v84, s[20:21] offset:3072 sc1
	global_store_dword v39, v85, s[22:23] offset:3072 sc1
	global_store_dword v39, v86, s[24:25] offset:3072 sc1
	global_store_dword v39, v87, s[26:27] offset:3072 sc1
	s_add_u32 s20, s20, 0x1000
	s_addc_u32 s21, s21, 0
	s_add_u32 s22, s22, 0x1000
	s_addc_u32 s23, s23, 0
	s_add_u32 s24, s24, 0x1000
	s_addc_u32 s25, s25, 0
	s_add_u32 s26, s26, 0x1000
	s_addc_u32 s27, s27, 0
	global_store_dword v39, v88, s[20:21] sc1
	global_store_dword v39, v89, s[22:23] sc1
	global_store_dword v39, v90, s[24:25] sc1
	global_store_dword v39, v91, s[26:27] sc1
	global_store_dword v39, v92, s[20:21] offset:1024 sc1
	global_store_dword v39, v93, s[22:23] offset:1024 sc1
	global_store_dword v39, v94, s[24:25] offset:1024 sc1
	global_store_dword v39, v95, s[26:27] offset:1024 sc1
	global_store_dword v39, v96, s[20:21] offset:2048 sc1
	global_store_dword v39, v97, s[22:23] offset:2048 sc1
	global_store_dword v39, v98, s[24:25] offset:2048 sc1
	global_store_dword v39, v99, s[26:27] offset:2048 sc1
	global_store_dword v39, v100, s[20:21] offset:3072 sc1
	global_store_dword v39, v101, s[22:23] offset:3072 sc1
	global_store_dword v39, v102, s[24:25] offset:3072 sc1
	global_store_dword v39, v103, s[26:27] offset:3072 sc1
	s_add_u32 s20, s20, 0x1000
	s_addc_u32 s21, s21, 0
	s_add_u32 s22, s22, 0x1000
	s_addc_u32 s23, s23, 0
	s_add_u32 s24, s24, 0x1000
	s_addc_u32 s25, s25, 0
	s_add_u32 s26, s26, 0x1000
	s_addc_u32 s27, s27, 0
	global_store_dword v39, v104, s[20:21] sc1
	global_store_dword v39, v105, s[22:23] sc1
	global_store_dword v39, v106, s[24:25] sc1
	global_store_dword v39, v107, s[26:27] sc1
	global_store_dword v39, v108, s[20:21] offset:1024 sc1
	global_store_dword v39, v109, s[22:23] offset:1024 sc1
	global_store_dword v39, v110, s[24:25] offset:1024 sc1
	global_store_dword v39, v111, s[26:27] offset:1024 sc1
	global_store_dword v39, v112, s[20:21] offset:2048 sc1
	global_store_dword v39, v113, s[22:23] offset:2048 sc1
	global_store_dword v39, v114, s[24:25] offset:2048 sc1
	global_store_dword v39, v115, s[26:27] offset:2048 sc1
	global_store_dword v39, v116, s[20:21] offset:3072 sc1
	global_store_dword v39, v117, s[22:23] offset:3072 sc1
	global_store_dword v39, v118, s[24:25] offset:3072 sc1
	global_store_dword v39, v119, s[26:27] offset:3072 sc1
	s_add_u32 s20, s20, 0x1000
	s_addc_u32 s21, s21, 0
	s_add_u32 s22, s22, 0x1000
	s_addc_u32 s23, s23, 0
	s_add_u32 s24, s24, 0x1000
	s_addc_u32 s25, s25, 0
	s_add_u32 s26, s26, 0x1000
	s_addc_u32 s27, s27, 0
	global_store_dword v39, v120, s[20:21] sc1
	global_store_dword v39, v121, s[22:23] sc1
	global_store_dword v39, v122, s[24:25] sc1
	global_store_dword v39, v123, s[26:27] sc1
	global_store_dword v39, v124, s[20:21] offset:1024 sc1
	global_store_dword v39, v125, s[22:23] offset:1024 sc1
	global_store_dword v39, v126, s[24:25] offset:1024 sc1
	global_store_dword v39, v127, s[26:27] offset:1024 sc1
	global_store_dword v39, v36, s[20:21] offset:2048 sc1
	global_store_dword v39, v37, s[22:23] offset:2048 sc1
	global_store_dword v39, v45, s[24:25] offset:2048 sc1
	global_store_dword v39, v46, s[26:27] offset:2048 sc1
	global_store_dword v39, v53, s[20:21] offset:3072 sc1
	global_store_dword v39, v54, s[22:23] offset:3072 sc1
	global_store_dword v39, v55, s[24:25] offset:3072 sc1
	global_store_dword v39, v1, s[26:27] offset:3072 sc1
	v_mul_f32_e32 v40, 0x3c010204, v40
	v_and_b32_e32 v42, 63, v0
	v_lshlrev_b32_e32 v41, 5, v42
	s_add_u32 s15, s12, s14
	s_lshl_b32 s15, s15, 2
	s_add_u32 s8, s8, s15
	s_addc_u32 s9, s9, 0
	s_add_u32 s15, s29, 24
	v_cmp_gt_u32_e32 vcc, s15, v42
	s_and_saveexec_b64 s[38:39], vcc
	global_store_dword v41, v40, s[8:9]
	s_mov_b64 exec, s[38:39]
	s_lshl_b32 s15, s14, 12
	v_add_u32_e32 v41, s15, v34
	s_barrier
	ds_write_b128 v41, v[2:5]
	ds_write_b128 v41, v[6:9] offset:1024
	ds_write_b128 v41, v[10:13] offset:2048
	ds_write_b128 v41, v[14:17] offset:3072
	s_waitcnt lgkmcnt(0)
	s_barrier
	s_movk_i32 s15, 0x100
	v_cmp_gt_u32_e32 vcc, s15, v0
	s_and_saveexec_b64 s[38:39], vcc
	s_cbranch_execz .Lk1_end
	v_lshlrev_b32_e32 v16, 4, v0
	ds_read_b128 v[2:5], v16
	ds_read_b128 v[18:21], v16 offset:4096
	ds_read_b128 v[22:25], v16 offset:8192
	ds_read_b128 v[26:29], v16 offset:12288
	ds_read_b128 v[30:33], v16 offset:16384
	ds_read_b128 v[34:37], v16 offset:20480
	ds_read_b128 v[38:41], v16 offset:24576
	ds_read_b128 v[42:45], v16 offset:28672
	s_waitcnt lgkmcnt(6)
	v_pk_add_f32 v[2:3], v[2:3], v[18:19]
	v_pk_add_f32 v[4:5], v[4:5], v[20:21]
	s_waitcnt lgkmcnt(5)
	v_pk_add_f32 v[2:3], v[2:3], v[22:23]
	v_pk_add_f32 v[4:5], v[4:5], v[24:25]
	s_waitcnt lgkmcnt(4)
	v_pk_add_f32 v[2:3], v[2:3], v[26:27]
	v_pk_add_f32 v[4:5], v[4:5], v[28:29]
	s_waitcnt lgkmcnt(3)
	v_pk_add_f32 v[2:3], v[2:3], v[30:31]
	v_pk_add_f32 v[4:5], v[4:5], v[32:33]
	s_waitcnt lgkmcnt(2)
	v_pk_add_f32 v[2:3], v[2:3], v[34:35]
	v_pk_add_f32 v[4:5], v[4:5], v[36:37]
	s_waitcnt lgkmcnt(1)
	v_pk_add_f32 v[2:3], v[2:3], v[38:39]
	v_pk_add_f32 v[4:5], v[4:5], v[40:41]
	s_waitcnt lgkmcnt(0)
	v_pk_add_f32 v[2:3], v[2:3], v[42:43]
	v_pk_add_f32 v[4:5], v[4:5], v[44:45]
	s_lshl_b32 s15, s2, 12
	s_add_u32 s10, s10, s15
	s_addc_u32 s11, s11, 0
	global_store_dwordx4 v16, v[2:5], s[10:11]
